# GEMM K-loops: removed the compiler's lgkmcnt(0) at the head of each MFMA segment (already drained by the explicit wait before the barrier)
# speedup vs baseline: 1.0075x; 1.0075x over previous
.LBB0_121:
	s_add_u32 s38, s12, 0x80
	s_addc_u32 s39, s13, 0
	s_waitcnt vmcnt(8)
	s_and_b64 s[14:15], s[14:15], exec
	s_waitcnt lgkmcnt(0)
	s_cselect_b32 s14, s57, s58
	s_cselect_b32 s41, s31, s39
	s_cselect_b32 s40, s30, s38
	s_cselect_b32 s15, s7, s59
	s_add_u32 s38, s14, 0x8000
	s_addc_u32 s39, s15, 0
	s_barrier
	s_setprio 1
	v_mfma_f32_16x16x32_bf16 v[64:67], v[104:107], v[128:131], v[64:67]
	v_mfma_f32_16x16x32_bf16 v[60:63], v[112:115], v[128:131], v[60:63]
	v_mfma_f32_16x16x32_bf16 v[56:59], v[104:107], v[120:123], v[56:59]
	v_mfma_f32_16x16x32_bf16 v[52:55], v[112:115], v[120:123], v[52:55]
	v_mfma_f32_16x16x32_bf16 v[40:43], v[104:107], v[96:99], v[40:43]
	v_mfma_f32_16x16x32_bf16 v[36:39], v[112:115], v[96:99], v[36:39]
	v_mfma_f32_16x16x32_bf16 v[24:27], v[104:107], v[88:91], v[24:27]
	v_mfma_f32_16x16x32_bf16 v[20:23], v[112:115], v[88:91], v[20:23]
	v_mfma_f32_16x16x32_bf16 v[64:67], v[108:111], v[132:135], v[64:67]
	v_mfma_f32_16x16x32_bf16 v[60:63], v[116:119], v[132:135], v[60:63]
	v_mfma_f32_16x16x32_bf16 v[56:59], v[108:111], v[124:127], v[56:59]
	v_mfma_f32_16x16x32_bf16 v[52:55], v[116:119], v[124:127], v[52:55]
	v_mfma_f32_16x16x32_bf16 v[40:43], v[108:111], v[100:103], v[40:43]
	v_mfma_f32_16x16x32_bf16 v[36:39], v[116:119], v[100:103], v[36:39]
	v_mfma_f32_16x16x32_bf16 v[24:27], v[108:111], v[92:95], v[24:27]
	v_mfma_f32_16x16x32_bf16 v[20:23], v[116:119], v[92:95], v[20:23]
	s_setprio 0
	s_setprio 1
	v_mfma_f32_16x16x32_bf16 v[48:51], v[68:71], v[128:131], v[48:51]
	v_mfma_f32_16x16x32_bf16 v[44:47], v[76:79], v[128:131], v[44:47]
	v_mfma_f32_16x16x32_bf16 v[32:35], v[68:71], v[120:123], v[32:35]
	v_mfma_f32_16x16x32_bf16 v[28:31], v[76:79], v[120:123], v[28:31]
	v_mfma_f32_16x16x32_bf16 v[16:19], v[68:71], v[96:99], v[16:19]
	v_mfma_f32_16x16x32_bf16 v[12:15], v[76:79], v[96:99], v[12:15]
	v_mfma_f32_16x16x32_bf16 v[8:11], v[68:71], v[88:91], v[8:11]
	v_mfma_f32_16x16x32_bf16 v[4:7], v[76:79], v[88:91], v[4:7]
	v_mfma_f32_16x16x32_bf16 v[48:51], v[72:75], v[132:135], v[48:51]
	v_mfma_f32_16x16x32_bf16 v[44:47], v[80:83], v[132:135], v[44:47]
	v_mfma_f32_16x16x32_bf16 v[32:35], v[72:75], v[124:127], v[32:35]
	v_mfma_f32_16x16x32_bf16 v[28:31], v[80:83], v[124:127], v[28:31]
	v_mfma_f32_16x16x32_bf16 v[16:19], v[72:75], v[100:103], v[16:19]
	v_mfma_f32_16x16x32_bf16 v[12:15], v[80:83], v[100:103], v[12:15]
	v_mfma_f32_16x16x32_bf16 v[8:11], v[72:75], v[92:95], v[8:11]
	v_mfma_f32_16x16x32_bf16 v[4:7], v[80:83], v[92:95], v[4:7]
	s_setprio 0
	s_barrier
	s_mov_b32 m0, s43
	v_lshl_add_u64 v[68:69], s[14:15], 0, v[138:139]
	s_add_u32 s62, s14, 0x4000
	global_load_lds_dwordx4 v[68:69], off
	v_lshl_add_u64 v[68:69], s[14:15], 0, v[136:137]
	s_mov_b32 m0, s44
	s_addc_u32 s63, s15, 0
	global_load_lds_dwordx4 v[68:69], off
	v_lshl_add_u64 v[68:69], s[62:63], 0, v[138:139]
	s_mov_b32 m0, s45
	v_mov_b32_e32 v143, v3
	global_load_lds_dwordx4 v[68:69], off
	v_lshl_add_u64 v[68:69], s[62:63], 0, v[136:137]
	s_mov_b32 m0, s47
	v_lshl_add_u64 v[166:167], s[40:41], 0, v[2:3]
	global_load_lds_dwordx4 v[68:69], off
	s_mov_b32 m0, s42
	v_lshl_add_u64 v[168:169], s[40:41], 0, v[142:143]
	global_load_lds_dwordx4 v2, s[40:41]
	s_mov_b32 m0, s48
	s_nop 0
	global_load_lds_dwordx4 v142, s[40:41]
	s_waitcnt vmcnt(8)
	s_waitcnt lgkmcnt(0)
	s_barrier
	s_barrier
	s_add_i32 s61, 0, 0x18000
	s_add_i32 s62, 0, 0x1c000
	v_add_u32_e32 v80, s61, v160
	v_add_u32_e32 v100, s62, v160
	ds_read_b128 v[68:71], v80
	ds_read_b128 v[72:75], v80 offset:1024
	ds_read_b128 v[76:79], v80 offset:2048
	ds_read_b128 v[80:83], v80 offset:3072
	ds_read_b128 v[88:91], v100
	ds_read_b128 v[92:95], v100 offset:1024
	ds_read_b128 v[96:99], v100 offset:2048
	ds_read_b128 v[100:103], v100 offset:3072
	s_mov_b32 m0, s49
	v_lshl_add_u64 v[154:155], s[40:41], 0, v[154:155]
	ds_read_b128 v[104:107], v163 offset:32768
	ds_read_b128 v[108:111], v163 offset:33792
	ds_read_b128 v[112:115], v163 offset:34816
	ds_read_b128 v[116:119], v163 offset:35840
	ds_read_b128 v[120:123], v163 offset:36864
	ds_read_b128 v[124:127], v163 offset:37888
	ds_read_b128 v[128:131], v163 offset:38912
	ds_read_b128 v[132:135], v163 offset:39936
	global_load_lds_dwordx4 v[154:155], off
	v_lshl_add_u64 v[152:153], s[40:41], 0, v[152:153]
	s_mov_b32 m0, s50
	s_nop 0
	global_load_lds_dwordx4 v[152:153], off
	s_waitcnt vmcnt(8)
	s_waitcnt lgkmcnt(0)
	s_barrier
	s_setprio 1
	v_mfma_f32_16x16x32_bf16 v[64:67], v[68:71], v[104:107], v[64:67]
	v_mfma_f32_16x16x32_bf16 v[60:63], v[76:79], v[104:107], v[60:63]
	v_mfma_f32_16x16x32_bf16 v[56:59], v[68:71], v[112:115], v[56:59]
	v_mfma_f32_16x16x32_bf16 v[52:55], v[76:79], v[112:115], v[52:55]
	v_mfma_f32_16x16x32_bf16 v[40:43], v[68:71], v[120:123], v[40:43]
	v_mfma_f32_16x16x32_bf16 v[36:39], v[76:79], v[120:123], v[36:39]
	v_mfma_f32_16x16x32_bf16 v[24:27], v[68:71], v[128:131], v[24:27]
	v_mfma_f32_16x16x32_bf16 v[20:23], v[76:79], v[128:131], v[20:23]
	v_mfma_f32_16x16x32_bf16 v[64:67], v[72:75], v[108:111], v[64:67]
	v_mfma_f32_16x16x32_bf16 v[60:63], v[80:83], v[108:111], v[60:63]
	v_mfma_f32_16x16x32_bf16 v[56:59], v[72:75], v[116:119], v[56:59]
	v_mfma_f32_16x16x32_bf16 v[52:55], v[80:83], v[116:119], v[52:55]
	v_mfma_f32_16x16x32_bf16 v[40:43], v[72:75], v[124:127], v[40:43]
	v_mfma_f32_16x16x32_bf16 v[36:39], v[80:83], v[124:127], v[36:39]
	v_mfma_f32_16x16x32_bf16 v[24:27], v[72:75], v[132:135], v[24:27]
	v_mfma_f32_16x16x32_bf16 v[20:23], v[80:83], v[132:135], v[20:23]
	s_setprio 0
	s_setprio 1
	v_mfma_f32_16x16x32_bf16 v[48:51], v[88:91], v[104:107], v[48:51]
	v_mfma_f32_16x16x32_bf16 v[44:47], v[96:99], v[104:107], v[44:47]
	v_mfma_f32_16x16x32_bf16 v[32:35], v[88:91], v[112:115], v[32:35]
	v_mfma_f32_16x16x32_bf16 v[28:31], v[96:99], v[112:115], v[28:31]
	v_mfma_f32_16x16x32_bf16 v[16:19], v[88:91], v[120:123], v[16:19]
	v_mfma_f32_16x16x32_bf16 v[12:15], v[96:99], v[120:123], v[12:15]
	v_mfma_f32_16x16x32_bf16 v[8:11], v[88:91], v[128:131], v[8:11]
	v_mfma_f32_16x16x32_bf16 v[4:7], v[96:99], v[128:131], v[4:7]
	v_mfma_f32_16x16x32_bf16 v[48:51], v[92:95], v[108:111], v[48:51]
	v_mfma_f32_16x16x32_bf16 v[44:47], v[100:103], v[108:111], v[44:47]
	v_mfma_f32_16x16x32_bf16 v[32:35], v[92:95], v[116:119], v[32:35]
	v_mfma_f32_16x16x32_bf16 v[28:31], v[100:103], v[116:119], v[28:31]
	v_mfma_f32_16x16x32_bf16 v[16:19], v[92:95], v[124:127], v[16:19]
	v_mfma_f32_16x16x32_bf16 v[12:15], v[100:103], v[124:127], v[12:15]
	v_mfma_f32_16x16x32_bf16 v[8:11], v[92:95], v[132:135], v[8:11]
	v_mfma_f32_16x16x32_bf16 v[4:7], v[100:103], v[132:135], v[4:7]
	s_setprio 0
	s_barrier
	s_add_i32 s40, s61, s33
	v_lshl_add_u64 v[68:69], s[38:39], 0, v[138:139]
	s_mov_b32 m0, s40
	s_nop 0
	global_load_lds_dwordx4 v[68:69], off
	s_add_i32 m0, s40, 0x2000
	s_add_u32 s14, s14, 0xc000
	v_lshl_add_u64 v[68:69], s[38:39], 0, v[136:137]
	s_addc_u32 s15, s15, 0
	s_add_i32 s38, s62, s33
	global_load_lds_dwordx4 v[68:69], off
	v_lshl_add_u64 v[68:69], s[14:15], 0, v[138:139]
	s_mov_b32 m0, s38
	s_nop 0
	global_load_lds_dwordx4 v[68:69], off
	v_lshl_add_u64 v[68:69], s[14:15], 0, v[136:137]
	s_add_i32 m0, s38, 0x2000
	s_nop 0
	global_load_lds_dwordx4 v[68:69], off
	v_lshl_add_u64 v[68:69], v[166:167], 0, s[36:37]
	s_mov_b32 m0, s51
	s_nop 0
	global_load_lds_dwordx4 v[68:69], off
	v_lshl_add_u64 v[68:69], v[168:169], 0, s[36:37]
	s_mov_b32 m0, s52
	s_nop 0
	global_load_lds_dwordx4 v[68:69], off
	s_waitcnt vmcnt(8)
	s_waitcnt lgkmcnt(0)
	s_barrier
	s_barrier
	s_add_i32 s60, s60, 2
	s_add_u32 s58, s58, 0x10000
	s_addc_u32 s59, s59, 0
	s_add_u32 s12, s12, 0x100
	s_addc_u32 s13, s13, 0
	s_cmp_gt_u32 s60, 29
	s_cbranch_scc1 .LBB0_124

.LBB0_144:
	s_add_u32 s40, s14, 0x80
	s_addc_u32 s41, s15, 0
	s_waitcnt vmcnt(8)
	s_and_b64 s[38:39], s[38:39], exec
	s_waitcnt lgkmcnt(0)
	s_cselect_b32 s38, s13, s60
	s_cselect_b32 s43, s31, s41
	s_cselect_b32 s42, s30, s40
	s_cselect_b32 s39, s9, s61
	s_add_u32 s40, s38, 0x8000
	s_addc_u32 s41, s39, 0
	s_barrier
	s_setprio 1
	v_mfma_f32_16x16x32_bf16 v[132:135], v[152:155], v[192:195], v[132:135]
	v_mfma_f32_16x16x32_bf16 v[128:131], v[160:163], v[192:195], v[128:131]
	v_mfma_f32_16x16x32_bf16 v[124:127], v[152:155], v[184:187], v[124:127]
	v_mfma_f32_16x16x32_bf16 v[116:119], v[160:163], v[184:187], v[116:119]
	v_mfma_f32_16x16x32_bf16 v[108:111], v[152:155], v[176:179], v[108:111]
	v_mfma_f32_16x16x32_bf16 v[100:103], v[160:163], v[176:179], v[100:103]
	v_mfma_f32_16x16x32_bf16 v[92:95], v[152:155], v[168:171], v[92:95]
	v_mfma_f32_16x16x32_bf16 v[80:83], v[160:163], v[168:171], v[80:83]
	v_mfma_f32_16x16x32_bf16 v[132:135], v[156:159], v[196:199], v[132:135]
	v_mfma_f32_16x16x32_bf16 v[128:131], v[164:167], v[196:199], v[128:131]
	v_mfma_f32_16x16x32_bf16 v[124:127], v[156:159], v[188:191], v[124:127]
	v_mfma_f32_16x16x32_bf16 v[116:119], v[164:167], v[188:191], v[116:119]
	v_mfma_f32_16x16x32_bf16 v[108:111], v[156:159], v[180:183], v[108:111]
	v_mfma_f32_16x16x32_bf16 v[100:103], v[164:167], v[180:183], v[100:103]
	v_mfma_f32_16x16x32_bf16 v[92:95], v[156:159], v[172:175], v[92:95]
	v_mfma_f32_16x16x32_bf16 v[80:83], v[164:167], v[172:175], v[80:83]
	s_setprio 0
	s_setprio 1
	v_mfma_f32_16x16x32_bf16 v[120:123], v[136:139], v[192:195], v[120:123]
	v_mfma_f32_16x16x32_bf16 v[112:115], v[144:147], v[192:195], v[112:115]
	v_mfma_f32_16x16x32_bf16 v[104:107], v[136:139], v[184:187], v[104:107]
	v_mfma_f32_16x16x32_bf16 v[96:99], v[144:147], v[184:187], v[96:99]
	v_mfma_f32_16x16x32_bf16 v[88:91], v[136:139], v[176:179], v[88:91]
	v_mfma_f32_16x16x32_bf16 v[76:79], v[144:147], v[176:179], v[76:79]
	v_mfma_f32_16x16x32_bf16 v[72:75], v[136:139], v[168:171], v[72:75]
	v_mfma_f32_16x16x32_bf16 v[68:71], v[144:147], v[168:171], v[68:71]
	v_mfma_f32_16x16x32_bf16 v[120:123], v[140:143], v[196:199], v[120:123]
	v_mfma_f32_16x16x32_bf16 v[112:115], v[148:151], v[196:199], v[112:115]
	v_mfma_f32_16x16x32_bf16 v[104:107], v[140:143], v[188:191], v[104:107]
	v_mfma_f32_16x16x32_bf16 v[96:99], v[148:151], v[188:191], v[96:99]
	v_mfma_f32_16x16x32_bf16 v[88:91], v[140:143], v[180:183], v[88:91]
	v_mfma_f32_16x16x32_bf16 v[76:79], v[148:151], v[180:183], v[76:79]
	v_mfma_f32_16x16x32_bf16 v[72:75], v[140:143], v[172:175], v[72:75]
	v_mfma_f32_16x16x32_bf16 v[68:71], v[148:151], v[172:175], v[68:71]
	s_setprio 0
	s_barrier
	s_mov_b32 m0, s48
	v_lshl_add_u64 v[204:205], s[38:39], 0, v[210:211]
	s_add_u32 s64, s38, 0x4000
	ds_read_b128 v[168:171], v244 offset:16384
	ds_read_b128 v[172:175], v244 offset:17408
	ds_read_b128 v[176:179], v244 offset:18432
	ds_read_b128 v[180:183], v244 offset:19456
	ds_read_b128 v[184:187], v244 offset:20480
	ds_read_b128 v[188:191], v244 offset:21504
	ds_read_b128 v[192:195], v244 offset:22528
	ds_read_b128 v[196:199], v244 offset:23552
	global_load_lds_dwordx4 v[204:205], off
	v_lshl_add_u64 v[204:205], s[38:39], 0, v[208:209]
	s_mov_b32 m0, s49
	s_addc_u32 s65, s39, 0
	global_load_lds_dwordx4 v[204:205], off
	v_lshl_add_u64 v[204:205], s[64:65], 0, v[210:211]
	s_mov_b32 m0, s50
	v_mov_b32_e32 v215, v3
	global_load_lds_dwordx4 v[204:205], off
	v_lshl_add_u64 v[204:205], s[64:65], 0, v[208:209]
	s_mov_b32 m0, s51
	v_lshl_add_u64 v[248:249], s[42:43], 0, v[214:215]
	global_load_lds_dwordx4 v[204:205], off
	s_mov_b32 m0, s47
	v_lshl_add_u64 v[204:205], s[42:43], 0, v[2:3]
	global_load_lds_dwordx4 v2, s[42:43]
	s_mov_b32 m0, s52
	s_nop 0
	global_load_lds_dwordx4 v214, s[42:43]
	s_waitcnt vmcnt(8)
	s_waitcnt lgkmcnt(0)
	s_barrier
	s_setprio 1
	v_mfma_f32_16x16x32_bf16 v[64:67], v[152:155], v[168:171], v[64:67]
	v_mfma_f32_16x16x32_bf16 v[60:63], v[160:163], v[168:171], v[60:63]
	v_mfma_f32_16x16x32_bf16 v[56:59], v[152:155], v[176:179], v[56:59]
	v_mfma_f32_16x16x32_bf16 v[48:51], v[160:163], v[176:179], v[48:51]
	v_mfma_f32_16x16x32_bf16 v[40:43], v[152:155], v[184:187], v[40:43]
	v_mfma_f32_16x16x32_bf16 v[32:35], v[160:163], v[184:187], v[32:35]
	v_mfma_f32_16x16x32_bf16 v[24:27], v[152:155], v[192:195], v[24:27]
	v_mfma_f32_16x16x32_bf16 v[16:19], v[160:163], v[192:195], v[16:19]
	v_mfma_f32_16x16x32_bf16 v[64:67], v[156:159], v[172:175], v[64:67]
	v_mfma_f32_16x16x32_bf16 v[60:63], v[164:167], v[172:175], v[60:63]
	v_mfma_f32_16x16x32_bf16 v[56:59], v[156:159], v[180:183], v[56:59]
	v_mfma_f32_16x16x32_bf16 v[48:51], v[164:167], v[180:183], v[48:51]
	v_mfma_f32_16x16x32_bf16 v[40:43], v[156:159], v[188:191], v[40:43]
	v_mfma_f32_16x16x32_bf16 v[32:35], v[164:167], v[188:191], v[32:35]
	v_mfma_f32_16x16x32_bf16 v[24:27], v[156:159], v[196:199], v[24:27]
	v_mfma_f32_16x16x32_bf16 v[16:19], v[164:167], v[196:199], v[16:19]
	s_setprio 0
	s_setprio 1
	v_mfma_f32_16x16x32_bf16 v[52:55], v[136:139], v[168:171], v[52:55]
	v_mfma_f32_16x16x32_bf16 v[44:47], v[144:147], v[168:171], v[44:47]
	v_mfma_f32_16x16x32_bf16 v[36:39], v[136:139], v[176:179], v[36:39]
	v_mfma_f32_16x16x32_bf16 v[28:31], v[144:147], v[176:179], v[28:31]
	v_mfma_f32_16x16x32_bf16 v[20:23], v[136:139], v[184:187], v[20:23]
	v_mfma_f32_16x16x32_bf16 v[12:15], v[144:147], v[184:187], v[12:15]
	v_mfma_f32_16x16x32_bf16 v[8:11], v[136:139], v[192:195], v[8:11]
	v_mfma_f32_16x16x32_bf16 v[4:7], v[144:147], v[192:195], v[4:7]
	v_mfma_f32_16x16x32_bf16 v[52:55], v[140:143], v[172:175], v[52:55]
	v_mfma_f32_16x16x32_bf16 v[44:47], v[148:151], v[172:175], v[44:47]
	v_mfma_f32_16x16x32_bf16 v[36:39], v[140:143], v[180:183], v[36:39]
	v_mfma_f32_16x16x32_bf16 v[28:31], v[148:151], v[180:183], v[28:31]
	v_mfma_f32_16x16x32_bf16 v[20:23], v[140:143], v[188:191], v[20:23]
	v_mfma_f32_16x16x32_bf16 v[12:15], v[148:151], v[188:191], v[12:15]
	v_mfma_f32_16x16x32_bf16 v[8:11], v[140:143], v[196:199], v[8:11]
	v_mfma_f32_16x16x32_bf16 v[4:7], v[148:151], v[196:199], v[4:7]
	s_setprio 0
	s_barrier
	s_add_i32 s63, 0, 0x18000
	s_add_i32 s64, 0, 0x1c000
	v_add_u32_e32 v148, s63, v243
	v_add_u32_e32 v164, s64, v243
	ds_read_b128 v[136:139], v148
	ds_read_b128 v[140:143], v148 offset:1024
	ds_read_b128 v[144:147], v148 offset:2048
	ds_read_b128 v[148:151], v148 offset:3072
	ds_read_b128 v[152:155], v164
	ds_read_b128 v[156:159], v164 offset:1024
	ds_read_b128 v[160:163], v164 offset:2048
	ds_read_b128 v[164:167], v164 offset:3072
	s_mov_b32 m0, s53
	v_lshl_add_u64 v[226:227], s[42:43], 0, v[226:227]
	ds_read_b128 v[168:171], v244 offset:32768
	ds_read_b128 v[172:175], v244 offset:33792
	ds_read_b128 v[176:179], v244 offset:34816
	ds_read_b128 v[180:183], v244 offset:35840
	ds_read_b128 v[184:187], v244 offset:36864
	ds_read_b128 v[188:191], v244 offset:37888
	ds_read_b128 v[192:195], v244 offset:38912
	ds_read_b128 v[196:199], v244 offset:39936
	global_load_lds_dwordx4 v[226:227], off
	v_lshl_add_u64 v[224:225], s[42:43], 0, v[224:225]
	s_mov_b32 m0, s54
	s_nop 0
	global_load_lds_dwordx4 v[224:225], off
	s_waitcnt vmcnt(8)
	s_waitcnt lgkmcnt(0)
	s_barrier
	s_setprio 1
	v_mfma_f32_16x16x32_bf16 v[132:135], v[136:139], v[168:171], v[132:135]
	v_mfma_f32_16x16x32_bf16 v[128:131], v[144:147], v[168:171], v[128:131]
	v_mfma_f32_16x16x32_bf16 v[124:127], v[136:139], v[176:179], v[124:127]
	v_mfma_f32_16x16x32_bf16 v[116:119], v[144:147], v[176:179], v[116:119]
	v_mfma_f32_16x16x32_bf16 v[108:111], v[136:139], v[184:187], v[108:111]
	v_mfma_f32_16x16x32_bf16 v[100:103], v[144:147], v[184:187], v[100:103]
	v_mfma_f32_16x16x32_bf16 v[92:95], v[136:139], v[192:195], v[92:95]
	v_mfma_f32_16x16x32_bf16 v[80:83], v[144:147], v[192:195], v[80:83]
	v_mfma_f32_16x16x32_bf16 v[132:135], v[140:143], v[172:175], v[132:135]
	v_mfma_f32_16x16x32_bf16 v[128:131], v[148:151], v[172:175], v[128:131]
	v_mfma_f32_16x16x32_bf16 v[124:127], v[140:143], v[180:183], v[124:127]
	v_mfma_f32_16x16x32_bf16 v[116:119], v[148:151], v[180:183], v[116:119]
	v_mfma_f32_16x16x32_bf16 v[108:111], v[140:143], v[188:191], v[108:111]
	v_mfma_f32_16x16x32_bf16 v[100:103], v[148:151], v[188:191], v[100:103]
	v_mfma_f32_16x16x32_bf16 v[92:95], v[140:143], v[196:199], v[92:95]
	v_mfma_f32_16x16x32_bf16 v[80:83], v[148:151], v[196:199], v[80:83]
	s_setprio 0
	s_setprio 1
	v_mfma_f32_16x16x32_bf16 v[120:123], v[152:155], v[168:171], v[120:123]
	v_mfma_f32_16x16x32_bf16 v[112:115], v[160:163], v[168:171], v[112:115]
	v_mfma_f32_16x16x32_bf16 v[104:107], v[152:155], v[176:179], v[104:107]
	v_mfma_f32_16x16x32_bf16 v[96:99], v[160:163], v[176:179], v[96:99]
	v_mfma_f32_16x16x32_bf16 v[88:91], v[152:155], v[184:187], v[88:91]
	v_mfma_f32_16x16x32_bf16 v[76:79], v[160:163], v[184:187], v[76:79]
	v_mfma_f32_16x16x32_bf16 v[72:75], v[152:155], v[192:195], v[72:75]
	v_mfma_f32_16x16x32_bf16 v[68:71], v[160:163], v[192:195], v[68:71]
	v_mfma_f32_16x16x32_bf16 v[120:123], v[156:159], v[172:175], v[120:123]
	v_mfma_f32_16x16x32_bf16 v[112:115], v[164:167], v[172:175], v[112:115]
	v_mfma_f32_16x16x32_bf16 v[104:107], v[156:159], v[180:183], v[104:107]
	v_mfma_f32_16x16x32_bf16 v[96:99], v[164:167], v[180:183], v[96:99]
	v_mfma_f32_16x16x32_bf16 v[88:91], v[156:159], v[188:191], v[88:91]
	v_mfma_f32_16x16x32_bf16 v[76:79], v[164:167], v[188:191], v[76:79]
	v_mfma_f32_16x16x32_bf16 v[72:75], v[156:159], v[196:199], v[72:75]
	v_mfma_f32_16x16x32_bf16 v[68:71], v[164:167], v[196:199], v[68:71]
	s_setprio 0
	s_barrier
	s_add_i32 s42, s63, s45
	v_lshl_add_u64 v[224:225], s[40:41], 0, v[210:211]
	s_mov_b32 m0, s42
	ds_read_b128 v[168:171], v244 offset:49152
	ds_read_b128 v[172:175], v244 offset:50176
	ds_read_b128 v[176:179], v244 offset:51200
	ds_read_b128 v[180:183], v244 offset:52224
	ds_read_b128 v[184:187], v244 offset:53248
	ds_read_b128 v[188:191], v244 offset:54272
	ds_read_b128 v[192:195], v244 offset:55296
	ds_read_b128 v[196:199], v244 offset:56320
	global_load_lds_dwordx4 v[224:225], off
	s_add_i32 m0, s42, 0x2000
	s_add_u32 s38, s38, 0xc000
	v_lshl_add_u64 v[224:225], s[40:41], 0, v[208:209]
	s_addc_u32 s39, s39, 0
	s_add_i32 s40, s64, s45
	global_load_lds_dwordx4 v[224:225], off
	v_lshl_add_u64 v[224:225], s[38:39], 0, v[210:211]
	s_mov_b32 m0, s40
	v_lshl_add_u64 v[204:205], v[204:205], 0, s[36:37]
	global_load_lds_dwordx4 v[224:225], off
	v_lshl_add_u64 v[224:225], s[38:39], 0, v[208:209]
	s_add_i32 m0, s40, 0x2000
	s_nop 0
	global_load_lds_dwordx4 v[224:225], off
	s_mov_b32 m0, s55
	s_nop 0
	global_load_lds_dwordx4 v[204:205], off
	v_lshl_add_u64 v[204:205], v[248:249], 0, s[36:37]
	s_mov_b32 m0, s56
	s_nop 0
	global_load_lds_dwordx4 v[204:205], off
	s_waitcnt vmcnt(8)
	s_waitcnt lgkmcnt(0)
	s_barrier
	s_setprio 1
	v_mfma_f32_16x16x32_bf16 v[64:67], v[136:139], v[168:171], v[64:67]
	v_mfma_f32_16x16x32_bf16 v[60:63], v[144:147], v[168:171], v[60:63]
	v_mfma_f32_16x16x32_bf16 v[56:59], v[136:139], v[176:179], v[56:59]
	v_mfma_f32_16x16x32_bf16 v[48:51], v[144:147], v[176:179], v[48:51]
	v_mfma_f32_16x16x32_bf16 v[40:43], v[136:139], v[184:187], v[40:43]
	v_mfma_f32_16x16x32_bf16 v[32:35], v[144:147], v[184:187], v[32:35]
	v_mfma_f32_16x16x32_bf16 v[24:27], v[136:139], v[192:195], v[24:27]
	v_mfma_f32_16x16x32_bf16 v[16:19], v[144:147], v[192:195], v[16:19]
	v_mfma_f32_16x16x32_bf16 v[64:67], v[140:143], v[172:175], v[64:67]
	v_mfma_f32_16x16x32_bf16 v[60:63], v[148:151], v[172:175], v[60:63]
	v_mfma_f32_16x16x32_bf16 v[56:59], v[140:143], v[180:183], v[56:59]
	v_mfma_f32_16x16x32_bf16 v[48:51], v[148:151], v[180:183], v[48:51]
	v_mfma_f32_16x16x32_bf16 v[40:43], v[140:143], v[188:191], v[40:43]
	v_mfma_f32_16x16x32_bf16 v[32:35], v[148:151], v[188:191], v[32:35]
	v_mfma_f32_16x16x32_bf16 v[24:27], v[140:143], v[196:199], v[24:27]
	v_mfma_f32_16x16x32_bf16 v[16:19], v[148:151], v[196:199], v[16:19]
	s_setprio 0
	s_setprio 1
	v_mfma_f32_16x16x32_bf16 v[52:55], v[152:155], v[168:171], v[52:55]
	v_mfma_f32_16x16x32_bf16 v[44:47], v[160:163], v[168:171], v[44:47]
	v_mfma_f32_16x16x32_bf16 v[36:39], v[152:155], v[176:179], v[36:39]
	v_mfma_f32_16x16x32_bf16 v[28:31], v[160:163], v[176:179], v[28:31]
	v_mfma_f32_16x16x32_bf16 v[20:23], v[152:155], v[184:187], v[20:23]
	v_mfma_f32_16x16x32_bf16 v[12:15], v[160:163], v[184:187], v[12:15]
	v_mfma_f32_16x16x32_bf16 v[8:11], v[152:155], v[192:195], v[8:11]
	v_mfma_f32_16x16x32_bf16 v[4:7], v[160:163], v[192:195], v[4:7]
	v_mfma_f32_16x16x32_bf16 v[52:55], v[156:159], v[172:175], v[52:55]
	v_mfma_f32_16x16x32_bf16 v[44:47], v[164:167], v[172:175], v[44:47]
	v_mfma_f32_16x16x32_bf16 v[36:39], v[156:159], v[180:183], v[36:39]
	v_mfma_f32_16x16x32_bf16 v[28:31], v[164:167], v[180:183], v[28:31]
	v_mfma_f32_16x16x32_bf16 v[20:23], v[156:159], v[188:191], v[20:23]
	v_mfma_f32_16x16x32_bf16 v[12:15], v[164:167], v[188:191], v[12:15]
	v_mfma_f32_16x16x32_bf16 v[8:11], v[156:159], v[196:199], v[8:11]
	v_mfma_f32_16x16x32_bf16 v[4:7], v[164:167], v[196:199], v[4:7]
	s_setprio 0
	s_barrier
	s_add_i32 s62, s62, 2
	s_add_u32 s60, s60, 0x10000
	s_addc_u32 s61, s61, 0
	s_add_u32 s14, s14, 0x100
	s_addc_u32 s15, s15, 0
	s_cmp_gt_u32 s62, 29
	s_cbranch_scc1 .LBB0_147

.LBB0_294:
	s_add_u32 s40, s14, 0x80
	s_addc_u32 s41, s15, 0
	s_waitcnt vmcnt(8)
	s_and_b64 s[38:39], s[38:39], exec
	s_waitcnt lgkmcnt(0)
	s_cselect_b32 s38, s13, s59
	s_cselect_b32 s43, s1, s41
	s_cselect_b32 s42, s0, s40
	s_cselect_b32 s39, s9, s60
	s_add_u32 s40, s38, 0x8000
	s_addc_u32 s41, s39, 0
	s_barrier
	s_setprio 1
	v_mfma_f32_16x16x32_bf16 v[132:135], v[152:155], v[192:195], v[132:135]
	v_mfma_f32_16x16x32_bf16 v[128:131], v[160:163], v[192:195], v[128:131]
	v_mfma_f32_16x16x32_bf16 v[124:127], v[152:155], v[184:187], v[124:127]
	v_mfma_f32_16x16x32_bf16 v[120:123], v[160:163], v[184:187], v[120:123]
	v_mfma_f32_16x16x32_bf16 v[108:111], v[152:155], v[176:179], v[108:111]
	v_mfma_f32_16x16x32_bf16 v[104:107], v[160:163], v[176:179], v[104:107]
	v_mfma_f32_16x16x32_bf16 v[92:95], v[152:155], v[168:171], v[92:95]
	v_mfma_f32_16x16x32_bf16 v[88:91], v[160:163], v[168:171], v[88:91]
	v_mfma_f32_16x16x32_bf16 v[132:135], v[156:159], v[196:199], v[132:135]
	v_mfma_f32_16x16x32_bf16 v[128:131], v[164:167], v[196:199], v[128:131]
	v_mfma_f32_16x16x32_bf16 v[124:127], v[156:159], v[188:191], v[124:127]
	v_mfma_f32_16x16x32_bf16 v[120:123], v[164:167], v[188:191], v[120:123]
	v_mfma_f32_16x16x32_bf16 v[108:111], v[156:159], v[180:183], v[108:111]
	v_mfma_f32_16x16x32_bf16 v[104:107], v[164:167], v[180:183], v[104:107]
	v_mfma_f32_16x16x32_bf16 v[92:95], v[156:159], v[172:175], v[92:95]
	v_mfma_f32_16x16x32_bf16 v[88:91], v[164:167], v[172:175], v[88:91]
	s_setprio 0
	s_setprio 1
	v_mfma_f32_16x16x32_bf16 v[116:119], v[136:139], v[192:195], v[116:119]
	v_mfma_f32_16x16x32_bf16 v[112:115], v[144:147], v[192:195], v[112:115]
	v_mfma_f32_16x16x32_bf16 v[100:103], v[136:139], v[184:187], v[100:103]
	v_mfma_f32_16x16x32_bf16 v[96:99], v[144:147], v[184:187], v[96:99]
	v_mfma_f32_16x16x32_bf16 v[80:83], v[136:139], v[176:179], v[80:83]
	v_mfma_f32_16x16x32_bf16 v[76:79], v[144:147], v[176:179], v[76:79]
	v_mfma_f32_16x16x32_bf16 v[72:75], v[136:139], v[168:171], v[72:75]
	v_mfma_f32_16x16x32_bf16 v[68:71], v[144:147], v[168:171], v[68:71]
	v_mfma_f32_16x16x32_bf16 v[116:119], v[140:143], v[196:199], v[116:119]
	v_mfma_f32_16x16x32_bf16 v[112:115], v[148:151], v[196:199], v[112:115]
	v_mfma_f32_16x16x32_bf16 v[100:103], v[140:143], v[188:191], v[100:103]
	v_mfma_f32_16x16x32_bf16 v[96:99], v[148:151], v[188:191], v[96:99]
	v_mfma_f32_16x16x32_bf16 v[80:83], v[140:143], v[180:183], v[80:83]
	v_mfma_f32_16x16x32_bf16 v[76:79], v[148:151], v[180:183], v[76:79]
	v_mfma_f32_16x16x32_bf16 v[72:75], v[140:143], v[172:175], v[72:75]
	v_mfma_f32_16x16x32_bf16 v[68:71], v[148:151], v[172:175], v[68:71]
	s_setprio 0
	s_barrier
	s_mov_b32 m0, s47
	v_lshl_add_u64 v[204:205], s[38:39], 0, v[210:211]
	s_add_u32 s62, s38, 0x4000
	ds_read_b128 v[168:171], v244 offset:16384
	ds_read_b128 v[172:175], v244 offset:17408
	ds_read_b128 v[176:179], v244 offset:18432
	ds_read_b128 v[180:183], v244 offset:19456
	ds_read_b128 v[184:187], v244 offset:20480
	ds_read_b128 v[188:191], v244 offset:21504
	ds_read_b128 v[192:195], v244 offset:22528
	ds_read_b128 v[196:199], v244 offset:23552
	global_load_lds_dwordx4 v[204:205], off
	v_lshl_add_u64 v[204:205], s[38:39], 0, v[208:209]
	s_mov_b32 m0, s48
	s_addc_u32 s63, s39, 0
	global_load_lds_dwordx4 v[204:205], off
	v_lshl_add_u64 v[204:205], s[62:63], 0, v[210:211]
	s_mov_b32 m0, s49
	v_mov_b32_e32 v215, v3
	global_load_lds_dwordx4 v[204:205], off
	v_lshl_add_u64 v[204:205], s[62:63], 0, v[208:209]
	s_mov_b32 m0, s50
	v_lshl_add_u64 v[248:249], s[42:43], 0, v[214:215]
	global_load_lds_dwordx4 v[204:205], off
	s_mov_b32 m0, s45
	v_lshl_add_u64 v[204:205], s[42:43], 0, v[2:3]
	global_load_lds_dwordx4 v2, s[42:43]
	s_mov_b32 m0, s51
	s_nop 0
	global_load_lds_dwordx4 v214, s[42:43]
	s_waitcnt vmcnt(8)
	s_waitcnt lgkmcnt(0)
	s_barrier
	s_setprio 1
	v_mfma_f32_16x16x32_bf16 v[64:67], v[152:155], v[168:171], v[64:67]
	v_mfma_f32_16x16x32_bf16 v[60:63], v[160:163], v[168:171], v[60:63]
	v_mfma_f32_16x16x32_bf16 v[56:59], v[152:155], v[176:179], v[56:59]
	v_mfma_f32_16x16x32_bf16 v[52:55], v[160:163], v[176:179], v[52:55]
	v_mfma_f32_16x16x32_bf16 v[40:43], v[152:155], v[184:187], v[40:43]
	v_mfma_f32_16x16x32_bf16 v[36:39], v[160:163], v[184:187], v[36:39]
	v_mfma_f32_16x16x32_bf16 v[24:27], v[152:155], v[192:195], v[24:27]
	v_mfma_f32_16x16x32_bf16 v[20:23], v[160:163], v[192:195], v[20:23]
	v_mfma_f32_16x16x32_bf16 v[64:67], v[156:159], v[172:175], v[64:67]
	v_mfma_f32_16x16x32_bf16 v[60:63], v[164:167], v[172:175], v[60:63]
	v_mfma_f32_16x16x32_bf16 v[56:59], v[156:159], v[180:183], v[56:59]
	v_mfma_f32_16x16x32_bf16 v[52:55], v[164:167], v[180:183], v[52:55]
	v_mfma_f32_16x16x32_bf16 v[40:43], v[156:159], v[188:191], v[40:43]
	v_mfma_f32_16x16x32_bf16 v[36:39], v[164:167], v[188:191], v[36:39]
	v_mfma_f32_16x16x32_bf16 v[24:27], v[156:159], v[196:199], v[24:27]
	v_mfma_f32_16x16x32_bf16 v[20:23], v[164:167], v[196:199], v[20:23]
	s_setprio 0
	s_setprio 1
	v_mfma_f32_16x16x32_bf16 v[48:51], v[136:139], v[168:171], v[48:51]
	v_mfma_f32_16x16x32_bf16 v[44:47], v[144:147], v[168:171], v[44:47]
	v_mfma_f32_16x16x32_bf16 v[32:35], v[136:139], v[176:179], v[32:35]
	v_mfma_f32_16x16x32_bf16 v[28:31], v[144:147], v[176:179], v[28:31]
	v_mfma_f32_16x16x32_bf16 v[16:19], v[136:139], v[184:187], v[16:19]
	v_mfma_f32_16x16x32_bf16 v[12:15], v[144:147], v[184:187], v[12:15]
	v_mfma_f32_16x16x32_bf16 v[8:11], v[136:139], v[192:195], v[8:11]
	v_mfma_f32_16x16x32_bf16 v[4:7], v[144:147], v[192:195], v[4:7]
	v_mfma_f32_16x16x32_bf16 v[48:51], v[140:143], v[172:175], v[48:51]
	v_mfma_f32_16x16x32_bf16 v[44:47], v[148:151], v[172:175], v[44:47]
	v_mfma_f32_16x16x32_bf16 v[32:35], v[140:143], v[180:183], v[32:35]
	v_mfma_f32_16x16x32_bf16 v[28:31], v[148:151], v[180:183], v[28:31]
	v_mfma_f32_16x16x32_bf16 v[16:19], v[140:143], v[188:191], v[16:19]
	v_mfma_f32_16x16x32_bf16 v[12:15], v[148:151], v[188:191], v[12:15]
	v_mfma_f32_16x16x32_bf16 v[8:11], v[140:143], v[196:199], v[8:11]
	v_mfma_f32_16x16x32_bf16 v[4:7], v[148:151], v[196:199], v[4:7]
	s_setprio 0
	s_barrier
	s_add_i32 s62, 0, 0x18000
	s_add_i32 s63, 0, 0x1c000
	v_add_u32_e32 v148, s62, v243
	v_add_u32_e32 v164, s63, v243
	ds_read_b128 v[136:139], v148
	ds_read_b128 v[140:143], v148 offset:1024
	ds_read_b128 v[144:147], v148 offset:2048
	ds_read_b128 v[148:151], v148 offset:3072
	ds_read_b128 v[152:155], v164
	ds_read_b128 v[156:159], v164 offset:1024
	ds_read_b128 v[160:163], v164 offset:2048
	ds_read_b128 v[164:167], v164 offset:3072
	s_mov_b32 m0, s52
	v_lshl_add_u64 v[226:227], s[42:43], 0, v[226:227]
	ds_read_b128 v[168:171], v244 offset:32768
	ds_read_b128 v[172:175], v244 offset:33792
	ds_read_b128 v[176:179], v244 offset:34816
	ds_read_b128 v[180:183], v244 offset:35840
	ds_read_b128 v[184:187], v244 offset:36864
	ds_read_b128 v[188:191], v244 offset:37888
	ds_read_b128 v[192:195], v244 offset:38912
	ds_read_b128 v[196:199], v244 offset:39936
	global_load_lds_dwordx4 v[226:227], off
	v_lshl_add_u64 v[224:225], s[42:43], 0, v[224:225]
	s_mov_b32 m0, s53
	s_nop 0
	global_load_lds_dwordx4 v[224:225], off
	s_waitcnt vmcnt(8)
	s_waitcnt lgkmcnt(0)
	s_barrier
	s_setprio 1
	v_mfma_f32_16x16x32_bf16 v[132:135], v[136:139], v[168:171], v[132:135]
	v_mfma_f32_16x16x32_bf16 v[128:131], v[144:147], v[168:171], v[128:131]
	v_mfma_f32_16x16x32_bf16 v[124:127], v[136:139], v[176:179], v[124:127]
	v_mfma_f32_16x16x32_bf16 v[120:123], v[144:147], v[176:179], v[120:123]
	v_mfma_f32_16x16x32_bf16 v[108:111], v[136:139], v[184:187], v[108:111]
	v_mfma_f32_16x16x32_bf16 v[104:107], v[144:147], v[184:187], v[104:107]
	v_mfma_f32_16x16x32_bf16 v[92:95], v[136:139], v[192:195], v[92:95]
	v_mfma_f32_16x16x32_bf16 v[88:91], v[144:147], v[192:195], v[88:91]
	v_mfma_f32_16x16x32_bf16 v[132:135], v[140:143], v[172:175], v[132:135]
	v_mfma_f32_16x16x32_bf16 v[128:131], v[148:151], v[172:175], v[128:131]
	v_mfma_f32_16x16x32_bf16 v[124:127], v[140:143], v[180:183], v[124:127]
	v_mfma_f32_16x16x32_bf16 v[120:123], v[148:151], v[180:183], v[120:123]
	v_mfma_f32_16x16x32_bf16 v[108:111], v[140:143], v[188:191], v[108:111]
	v_mfma_f32_16x16x32_bf16 v[104:107], v[148:151], v[188:191], v[104:107]
	v_mfma_f32_16x16x32_bf16 v[92:95], v[140:143], v[196:199], v[92:95]
	v_mfma_f32_16x16x32_bf16 v[88:91], v[148:151], v[196:199], v[88:91]
	s_setprio 0
	s_setprio 1
	v_mfma_f32_16x16x32_bf16 v[116:119], v[152:155], v[168:171], v[116:119]
	v_mfma_f32_16x16x32_bf16 v[112:115], v[160:163], v[168:171], v[112:115]
	v_mfma_f32_16x16x32_bf16 v[100:103], v[152:155], v[176:179], v[100:103]
	v_mfma_f32_16x16x32_bf16 v[96:99], v[160:163], v[176:179], v[96:99]
	v_mfma_f32_16x16x32_bf16 v[80:83], v[152:155], v[184:187], v[80:83]
	v_mfma_f32_16x16x32_bf16 v[76:79], v[160:163], v[184:187], v[76:79]
	v_mfma_f32_16x16x32_bf16 v[72:75], v[152:155], v[192:195], v[72:75]
	v_mfma_f32_16x16x32_bf16 v[68:71], v[160:163], v[192:195], v[68:71]
	v_mfma_f32_16x16x32_bf16 v[116:119], v[156:159], v[172:175], v[116:119]
	v_mfma_f32_16x16x32_bf16 v[112:115], v[164:167], v[172:175], v[112:115]
	v_mfma_f32_16x16x32_bf16 v[100:103], v[156:159], v[180:183], v[100:103]
	v_mfma_f32_16x16x32_bf16 v[96:99], v[164:167], v[180:183], v[96:99]
	v_mfma_f32_16x16x32_bf16 v[80:83], v[156:159], v[188:191], v[80:83]
	v_mfma_f32_16x16x32_bf16 v[76:79], v[164:167], v[188:191], v[76:79]
	v_mfma_f32_16x16x32_bf16 v[72:75], v[156:159], v[196:199], v[72:75]
	v_mfma_f32_16x16x32_bf16 v[68:71], v[164:167], v[196:199], v[68:71]
	s_setprio 0
	s_barrier
	s_add_i32 s42, s62, s44
	v_lshl_add_u64 v[224:225], s[40:41], 0, v[210:211]
	s_mov_b32 m0, s42
	ds_read_b128 v[168:171], v244 offset:49152
	ds_read_b128 v[172:175], v244 offset:50176
	ds_read_b128 v[176:179], v244 offset:51200
	ds_read_b128 v[180:183], v244 offset:52224
	ds_read_b128 v[184:187], v244 offset:53248
	ds_read_b128 v[188:191], v244 offset:54272
	ds_read_b128 v[192:195], v244 offset:55296
	ds_read_b128 v[196:199], v244 offset:56320
	global_load_lds_dwordx4 v[224:225], off
	s_add_i32 m0, s42, 0x2000
	s_add_u32 s38, s38, 0xc000
	v_lshl_add_u64 v[224:225], s[40:41], 0, v[208:209]
	s_addc_u32 s39, s39, 0
	s_add_i32 s40, s63, s44
	global_load_lds_dwordx4 v[224:225], off
	v_lshl_add_u64 v[224:225], s[38:39], 0, v[210:211]
	s_mov_b32 m0, s40
	v_lshl_add_u64 v[204:205], v[204:205], 0, s[36:37]
	global_load_lds_dwordx4 v[224:225], off
	v_lshl_add_u64 v[224:225], s[38:39], 0, v[208:209]
	s_add_i32 m0, s40, 0x2000
	s_nop 0
	global_load_lds_dwordx4 v[224:225], off
	s_mov_b32 m0, s54
	s_nop 0
	global_load_lds_dwordx4 v[204:205], off
	v_lshl_add_u64 v[204:205], v[248:249], 0, s[36:37]
	s_mov_b32 m0, s55
	s_nop 0
	global_load_lds_dwordx4 v[204:205], off
	s_waitcnt vmcnt(8)
	s_waitcnt lgkmcnt(0)
	s_barrier
	s_setprio 1
	v_mfma_f32_16x16x32_bf16 v[64:67], v[136:139], v[168:171], v[64:67]
	v_mfma_f32_16x16x32_bf16 v[60:63], v[144:147], v[168:171], v[60:63]
	v_mfma_f32_16x16x32_bf16 v[56:59], v[136:139], v[176:179], v[56:59]
	v_mfma_f32_16x16x32_bf16 v[52:55], v[144:147], v[176:179], v[52:55]
	v_mfma_f32_16x16x32_bf16 v[40:43], v[136:139], v[184:187], v[40:43]
	v_mfma_f32_16x16x32_bf16 v[36:39], v[144:147], v[184:187], v[36:39]
	v_mfma_f32_16x16x32_bf16 v[24:27], v[136:139], v[192:195], v[24:27]
	v_mfma_f32_16x16x32_bf16 v[20:23], v[144:147], v[192:195], v[20:23]
	v_mfma_f32_16x16x32_bf16 v[64:67], v[140:143], v[172:175], v[64:67]
	v_mfma_f32_16x16x32_bf16 v[60:63], v[148:151], v[172:175], v[60:63]
	v_mfma_f32_16x16x32_bf16 v[56:59], v[140:143], v[180:183], v[56:59]
	v_mfma_f32_16x16x32_bf16 v[52:55], v[148:151], v[180:183], v[52:55]
	v_mfma_f32_16x16x32_bf16 v[40:43], v[140:143], v[188:191], v[40:43]
	v_mfma_f32_16x16x32_bf16 v[36:39], v[148:151], v[188:191], v[36:39]
	v_mfma_f32_16x16x32_bf16 v[24:27], v[140:143], v[196:199], v[24:27]
	v_mfma_f32_16x16x32_bf16 v[20:23], v[148:151], v[196:199], v[20:23]
	s_setprio 0
	s_setprio 1
	v_mfma_f32_16x16x32_bf16 v[48:51], v[152:155], v[168:171], v[48:51]
	v_mfma_f32_16x16x32_bf16 v[44:47], v[160:163], v[168:171], v[44:47]
	v_mfma_f32_16x16x32_bf16 v[32:35], v[152:155], v[176:179], v[32:35]
	v_mfma_f32_16x16x32_bf16 v[28:31], v[160:163], v[176:179], v[28:31]
	v_mfma_f32_16x16x32_bf16 v[16:19], v[152:155], v[184:187], v[16:19]
	v_mfma_f32_16x16x32_bf16 v[12:15], v[160:163], v[184:187], v[12:15]
	v_mfma_f32_16x16x32_bf16 v[8:11], v[152:155], v[192:195], v[8:11]
	v_mfma_f32_16x16x32_bf16 v[4:7], v[160:163], v[192:195], v[4:7]
	v_mfma_f32_16x16x32_bf16 v[48:51], v[156:159], v[172:175], v[48:51]
	v_mfma_f32_16x16x32_bf16 v[44:47], v[164:167], v[172:175], v[44:47]
	v_mfma_f32_16x16x32_bf16 v[32:35], v[156:159], v[180:183], v[32:35]
	v_mfma_f32_16x16x32_bf16 v[28:31], v[164:167], v[180:183], v[28:31]
	v_mfma_f32_16x16x32_bf16 v[16:19], v[156:159], v[188:191], v[16:19]
	v_mfma_f32_16x16x32_bf16 v[12:15], v[164:167], v[188:191], v[12:15]
	v_mfma_f32_16x16x32_bf16 v[8:11], v[156:159], v[196:199], v[8:11]
	v_mfma_f32_16x16x32_bf16 v[4:7], v[164:167], v[196:199], v[4:7]
	s_setprio 0
	s_barrier
	s_add_i32 s61, s61, 2
	s_add_u32 s59, s59, 0x10000
	s_addc_u32 s60, s60, 0
	s_add_u32 s14, s14, 0x100
	s_addc_u32 s15, s15, 0
	s_cmp_gt_u32 s61, 29
	s_cbranch_scc1 .LBB0_297

.LBB0_498:
	s_add_u32 s38, s12, 0x80
	s_addc_u32 s39, s13, 0
	s_waitcnt vmcnt(8)
	s_and_b64 s[14:15], s[14:15], exec
	s_waitcnt lgkmcnt(0)
	s_cselect_b32 s14, s60, s61
	s_cselect_b32 s41, s31, s39
	s_cselect_b32 s40, s30, s38
	s_cselect_b32 s15, s9, s62
	s_add_u32 s38, s14, 0x8000
	s_addc_u32 s39, s15, 0
	s_barrier
	s_setprio 1
	v_mfma_f32_16x16x32_bf16 v[132:135], v[152:155], v[192:195], v[132:135]
	v_mfma_f32_16x16x32_bf16 v[128:131], v[160:163], v[192:195], v[128:131]
	v_mfma_f32_16x16x32_bf16 v[124:127], v[152:155], v[184:187], v[124:127]
	v_mfma_f32_16x16x32_bf16 v[120:123], v[160:163], v[184:187], v[120:123]
	v_mfma_f32_16x16x32_bf16 v[108:111], v[152:155], v[176:179], v[108:111]
	v_mfma_f32_16x16x32_bf16 v[104:107], v[160:163], v[176:179], v[104:107]
	v_mfma_f32_16x16x32_bf16 v[92:95], v[152:155], v[168:171], v[92:95]
	v_mfma_f32_16x16x32_bf16 v[88:91], v[160:163], v[168:171], v[88:91]
	v_mfma_f32_16x16x32_bf16 v[132:135], v[156:159], v[196:199], v[132:135]
	v_mfma_f32_16x16x32_bf16 v[128:131], v[164:167], v[196:199], v[128:131]
	v_mfma_f32_16x16x32_bf16 v[124:127], v[156:159], v[188:191], v[124:127]
	v_mfma_f32_16x16x32_bf16 v[120:123], v[164:167], v[188:191], v[120:123]
	v_mfma_f32_16x16x32_bf16 v[108:111], v[156:159], v[180:183], v[108:111]
	v_mfma_f32_16x16x32_bf16 v[104:107], v[164:167], v[180:183], v[104:107]
	v_mfma_f32_16x16x32_bf16 v[92:95], v[156:159], v[172:175], v[92:95]
	v_mfma_f32_16x16x32_bf16 v[88:91], v[164:167], v[172:175], v[88:91]
	s_setprio 0
	s_setprio 1
	v_mfma_f32_16x16x32_bf16 v[116:119], v[136:139], v[192:195], v[116:119]
	v_mfma_f32_16x16x32_bf16 v[112:115], v[144:147], v[192:195], v[112:115]
	v_mfma_f32_16x16x32_bf16 v[100:103], v[136:139], v[184:187], v[100:103]
	v_mfma_f32_16x16x32_bf16 v[96:99], v[144:147], v[184:187], v[96:99]
	v_mfma_f32_16x16x32_bf16 v[80:83], v[136:139], v[176:179], v[80:83]
	v_mfma_f32_16x16x32_bf16 v[76:79], v[144:147], v[176:179], v[76:79]
	v_mfma_f32_16x16x32_bf16 v[72:75], v[136:139], v[168:171], v[72:75]
	v_mfma_f32_16x16x32_bf16 v[68:71], v[144:147], v[168:171], v[68:71]
	v_mfma_f32_16x16x32_bf16 v[116:119], v[140:143], v[196:199], v[116:119]
	v_mfma_f32_16x16x32_bf16 v[112:115], v[148:151], v[196:199], v[112:115]
	v_mfma_f32_16x16x32_bf16 v[100:103], v[140:143], v[188:191], v[100:103]
	v_mfma_f32_16x16x32_bf16 v[96:99], v[148:151], v[188:191], v[96:99]
	v_mfma_f32_16x16x32_bf16 v[80:83], v[140:143], v[180:183], v[80:83]
	v_mfma_f32_16x16x32_bf16 v[76:79], v[148:151], v[180:183], v[76:79]
	v_mfma_f32_16x16x32_bf16 v[72:75], v[140:143], v[172:175], v[72:75]
	v_mfma_f32_16x16x32_bf16 v[68:71], v[148:151], v[172:175], v[68:71]
	s_setprio 0
	s_barrier
	s_mov_b32 m0, s44
	v_lshl_add_u64 v[246:247], s[14:15], 0, v[210:211]
	s_add_u32 s64, s14, 0x4000
	ds_read_b128 v[168:171], v243 offset:16384
	ds_read_b128 v[172:175], v243 offset:17408
	ds_read_b128 v[176:179], v243 offset:18432
	ds_read_b128 v[180:183], v243 offset:19456
	ds_read_b128 v[184:187], v243 offset:20480
	ds_read_b128 v[188:191], v243 offset:21504
	ds_read_b128 v[192:195], v243 offset:22528
	ds_read_b128 v[196:199], v243 offset:23552
	global_load_lds_dwordx4 v[246:247], off
	v_lshl_add_u64 v[246:247], s[14:15], 0, v[208:209]
	s_mov_b32 m0, s45
	s_addc_u32 s65, s15, 0
	global_load_lds_dwordx4 v[246:247], off
	v_lshl_add_u64 v[246:247], s[64:65], 0, v[210:211]
	s_mov_b32 m0, s47
	v_mov_b32_e32 v215, v3
	global_load_lds_dwordx4 v[246:247], off
	v_lshl_add_u64 v[246:247], s[64:65], 0, v[208:209]
	s_mov_b32 m0, s48
	v_lshl_add_u64 v[248:249], s[40:41], 0, v[214:215]
	global_load_lds_dwordx4 v[246:247], off
	s_mov_b32 m0, s43
	v_lshl_add_u64 v[246:247], s[40:41], 0, v[2:3]
	global_load_lds_dwordx4 v2, s[40:41]
	s_mov_b32 m0, s49
	s_nop 0
	global_load_lds_dwordx4 v214, s[40:41]
	s_waitcnt vmcnt(8)
	s_waitcnt lgkmcnt(0)
	s_barrier
	s_setprio 1
	v_mfma_f32_16x16x32_bf16 v[64:67], v[152:155], v[168:171], v[64:67]
	v_mfma_f32_16x16x32_bf16 v[60:63], v[160:163], v[168:171], v[60:63]
	v_mfma_f32_16x16x32_bf16 v[56:59], v[152:155], v[176:179], v[56:59]
	v_mfma_f32_16x16x32_bf16 v[52:55], v[160:163], v[176:179], v[52:55]
	v_mfma_f32_16x16x32_bf16 v[40:43], v[152:155], v[184:187], v[40:43]
	v_mfma_f32_16x16x32_bf16 v[36:39], v[160:163], v[184:187], v[36:39]
	v_mfma_f32_16x16x32_bf16 v[24:27], v[152:155], v[192:195], v[24:27]
	v_mfma_f32_16x16x32_bf16 v[20:23], v[160:163], v[192:195], v[20:23]
	v_mfma_f32_16x16x32_bf16 v[64:67], v[156:159], v[172:175], v[64:67]
	v_mfma_f32_16x16x32_bf16 v[60:63], v[164:167], v[172:175], v[60:63]
	v_mfma_f32_16x16x32_bf16 v[56:59], v[156:159], v[180:183], v[56:59]
	v_mfma_f32_16x16x32_bf16 v[52:55], v[164:167], v[180:183], v[52:55]
	v_mfma_f32_16x16x32_bf16 v[40:43], v[156:159], v[188:191], v[40:43]
	v_mfma_f32_16x16x32_bf16 v[36:39], v[164:167], v[188:191], v[36:39]
	v_mfma_f32_16x16x32_bf16 v[24:27], v[156:159], v[196:199], v[24:27]
	v_mfma_f32_16x16x32_bf16 v[20:23], v[164:167], v[196:199], v[20:23]
	s_setprio 0
	s_setprio 1
	v_mfma_f32_16x16x32_bf16 v[48:51], v[136:139], v[168:171], v[48:51]
	v_mfma_f32_16x16x32_bf16 v[44:47], v[144:147], v[168:171], v[44:47]
	v_mfma_f32_16x16x32_bf16 v[32:35], v[136:139], v[176:179], v[32:35]
	v_mfma_f32_16x16x32_bf16 v[28:31], v[144:147], v[176:179], v[28:31]
	v_mfma_f32_16x16x32_bf16 v[16:19], v[136:139], v[184:187], v[16:19]
	v_mfma_f32_16x16x32_bf16 v[12:15], v[144:147], v[184:187], v[12:15]
	v_mfma_f32_16x16x32_bf16 v[8:11], v[136:139], v[192:195], v[8:11]
	v_mfma_f32_16x16x32_bf16 v[4:7], v[144:147], v[192:195], v[4:7]
	v_mfma_f32_16x16x32_bf16 v[48:51], v[140:143], v[172:175], v[48:51]
	v_mfma_f32_16x16x32_bf16 v[44:47], v[148:151], v[172:175], v[44:47]
	v_mfma_f32_16x16x32_bf16 v[32:35], v[140:143], v[180:183], v[32:35]
	v_mfma_f32_16x16x32_bf16 v[28:31], v[148:151], v[180:183], v[28:31]
	v_mfma_f32_16x16x32_bf16 v[16:19], v[140:143], v[188:191], v[16:19]
	v_mfma_f32_16x16x32_bf16 v[12:15], v[148:151], v[188:191], v[12:15]
	v_mfma_f32_16x16x32_bf16 v[8:11], v[140:143], v[196:199], v[8:11]
	v_mfma_f32_16x16x32_bf16 v[4:7], v[148:151], v[196:199], v[4:7]
	s_setprio 0
	s_barrier
	s_add_i32 s64, 0, 0x18000
	s_add_i32 s65, 0, 0x1c000
	v_add_u32_e32 v148, s64, v241
	v_add_u32_e32 v164, s65, v241
	ds_read_b128 v[136:139], v148
	ds_read_b128 v[140:143], v148 offset:1024
	ds_read_b128 v[144:147], v148 offset:2048
	ds_read_b128 v[148:151], v148 offset:3072
	ds_read_b128 v[152:155], v164
	ds_read_b128 v[156:159], v164 offset:1024
	ds_read_b128 v[160:163], v164 offset:2048
	ds_read_b128 v[164:167], v164 offset:3072
	s_mov_b32 m0, s50
	v_lshl_add_u64 v[224:225], s[40:41], 0, v[224:225]
	ds_read_b128 v[168:171], v243 offset:32768
	ds_read_b128 v[172:175], v243 offset:33792
	ds_read_b128 v[176:179], v243 offset:34816
	ds_read_b128 v[180:183], v243 offset:35840
	ds_read_b128 v[184:187], v243 offset:36864
	ds_read_b128 v[188:191], v243 offset:37888
	ds_read_b128 v[192:195], v243 offset:38912
	ds_read_b128 v[196:199], v243 offset:39936
	global_load_lds_dwordx4 v[224:225], off
	v_lshl_add_u64 v[222:223], s[40:41], 0, v[222:223]
	s_mov_b32 m0, s51
	s_nop 0
	global_load_lds_dwordx4 v[222:223], off
	s_waitcnt vmcnt(8)
	s_waitcnt lgkmcnt(0)
	s_barrier
	s_setprio 1
	v_mfma_f32_16x16x32_bf16 v[132:135], v[136:139], v[168:171], v[132:135]
	v_mfma_f32_16x16x32_bf16 v[128:131], v[144:147], v[168:171], v[128:131]
	v_mfma_f32_16x16x32_bf16 v[124:127], v[136:139], v[176:179], v[124:127]
	v_mfma_f32_16x16x32_bf16 v[120:123], v[144:147], v[176:179], v[120:123]
	v_mfma_f32_16x16x32_bf16 v[108:111], v[136:139], v[184:187], v[108:111]
	v_mfma_f32_16x16x32_bf16 v[104:107], v[144:147], v[184:187], v[104:107]
	v_mfma_f32_16x16x32_bf16 v[92:95], v[136:139], v[192:195], v[92:95]
	v_mfma_f32_16x16x32_bf16 v[88:91], v[144:147], v[192:195], v[88:91]
	v_mfma_f32_16x16x32_bf16 v[132:135], v[140:143], v[172:175], v[132:135]
	v_mfma_f32_16x16x32_bf16 v[128:131], v[148:151], v[172:175], v[128:131]
	v_mfma_f32_16x16x32_bf16 v[124:127], v[140:143], v[180:183], v[124:127]
	v_mfma_f32_16x16x32_bf16 v[120:123], v[148:151], v[180:183], v[120:123]
	v_mfma_f32_16x16x32_bf16 v[108:111], v[140:143], v[188:191], v[108:111]
	v_mfma_f32_16x16x32_bf16 v[104:107], v[148:151], v[188:191], v[104:107]
	v_mfma_f32_16x16x32_bf16 v[92:95], v[140:143], v[196:199], v[92:95]
	v_mfma_f32_16x16x32_bf16 v[88:91], v[148:151], v[196:199], v[88:91]
	s_setprio 0
	s_setprio 1
	v_mfma_f32_16x16x32_bf16 v[116:119], v[152:155], v[168:171], v[116:119]
	v_mfma_f32_16x16x32_bf16 v[112:115], v[160:163], v[168:171], v[112:115]
	v_mfma_f32_16x16x32_bf16 v[100:103], v[152:155], v[176:179], v[100:103]
	v_mfma_f32_16x16x32_bf16 v[96:99], v[160:163], v[176:179], v[96:99]
	v_mfma_f32_16x16x32_bf16 v[80:83], v[152:155], v[184:187], v[80:83]
	v_mfma_f32_16x16x32_bf16 v[76:79], v[160:163], v[184:187], v[76:79]
	v_mfma_f32_16x16x32_bf16 v[72:75], v[152:155], v[192:195], v[72:75]
	v_mfma_f32_16x16x32_bf16 v[68:71], v[160:163], v[192:195], v[68:71]
	v_mfma_f32_16x16x32_bf16 v[116:119], v[156:159], v[172:175], v[116:119]
	v_mfma_f32_16x16x32_bf16 v[112:115], v[164:167], v[172:175], v[112:115]
	v_mfma_f32_16x16x32_bf16 v[100:103], v[156:159], v[180:183], v[100:103]
	v_mfma_f32_16x16x32_bf16 v[96:99], v[164:167], v[180:183], v[96:99]
	v_mfma_f32_16x16x32_bf16 v[80:83], v[156:159], v[188:191], v[80:83]
	v_mfma_f32_16x16x32_bf16 v[76:79], v[164:167], v[188:191], v[76:79]
	v_mfma_f32_16x16x32_bf16 v[72:75], v[156:159], v[196:199], v[72:75]
	v_mfma_f32_16x16x32_bf16 v[68:71], v[164:167], v[196:199], v[68:71]
	s_setprio 0
	s_barrier
	s_add_i32 s40, s64, s42
	v_lshl_add_u64 v[222:223], s[38:39], 0, v[210:211]
	s_mov_b32 m0, s40
	ds_read_b128 v[168:171], v243 offset:49152
	ds_read_b128 v[172:175], v243 offset:50176
	ds_read_b128 v[176:179], v243 offset:51200
	ds_read_b128 v[180:183], v243 offset:52224
	ds_read_b128 v[184:187], v243 offset:53248
	ds_read_b128 v[188:191], v243 offset:54272
	ds_read_b128 v[192:195], v243 offset:55296
	ds_read_b128 v[196:199], v243 offset:56320
	global_load_lds_dwordx4 v[222:223], off
	s_add_i32 m0, s40, 0x2000
	s_add_u32 s14, s14, 0xc000
	v_lshl_add_u64 v[222:223], s[38:39], 0, v[208:209]
	s_addc_u32 s15, s15, 0
	s_add_i32 s38, s65, s42
	global_load_lds_dwordx4 v[222:223], off
	v_lshl_add_u64 v[222:223], s[14:15], 0, v[210:211]
	s_mov_b32 m0, s38
	s_nop 0
	global_load_lds_dwordx4 v[222:223], off
	v_lshl_add_u64 v[222:223], s[14:15], 0, v[208:209]
	s_add_i32 m0, s38, 0x2000
	s_nop 0
	global_load_lds_dwordx4 v[222:223], off
	v_lshl_add_u64 v[222:223], v[246:247], 0, s[36:37]
	s_mov_b32 m0, s53
	s_nop 0
	global_load_lds_dwordx4 v[222:223], off
	v_lshl_add_u64 v[222:223], v[248:249], 0, s[36:37]
	s_mov_b32 m0, s54
	s_nop 0
	global_load_lds_dwordx4 v[222:223], off
	s_waitcnt vmcnt(8)
	s_waitcnt lgkmcnt(0)
	s_barrier
	s_setprio 1
	v_mfma_f32_16x16x32_bf16 v[64:67], v[136:139], v[168:171], v[64:67]
	v_mfma_f32_16x16x32_bf16 v[60:63], v[144:147], v[168:171], v[60:63]
	v_mfma_f32_16x16x32_bf16 v[56:59], v[136:139], v[176:179], v[56:59]
	v_mfma_f32_16x16x32_bf16 v[52:55], v[144:147], v[176:179], v[52:55]
	v_mfma_f32_16x16x32_bf16 v[40:43], v[136:139], v[184:187], v[40:43]
	v_mfma_f32_16x16x32_bf16 v[36:39], v[144:147], v[184:187], v[36:39]
	v_mfma_f32_16x16x32_bf16 v[24:27], v[136:139], v[192:195], v[24:27]
	v_mfma_f32_16x16x32_bf16 v[20:23], v[144:147], v[192:195], v[20:23]
	v_mfma_f32_16x16x32_bf16 v[64:67], v[140:143], v[172:175], v[64:67]
	v_mfma_f32_16x16x32_bf16 v[60:63], v[148:151], v[172:175], v[60:63]
	v_mfma_f32_16x16x32_bf16 v[56:59], v[140:143], v[180:183], v[56:59]
	v_mfma_f32_16x16x32_bf16 v[52:55], v[148:151], v[180:183], v[52:55]
	v_mfma_f32_16x16x32_bf16 v[40:43], v[140:143], v[188:191], v[40:43]
	v_mfma_f32_16x16x32_bf16 v[36:39], v[148:151], v[188:191], v[36:39]
	v_mfma_f32_16x16x32_bf16 v[24:27], v[140:143], v[196:199], v[24:27]
	v_mfma_f32_16x16x32_bf16 v[20:23], v[148:151], v[196:199], v[20:23]
	s_setprio 0
	s_setprio 1
	v_mfma_f32_16x16x32_bf16 v[48:51], v[152:155], v[168:171], v[48:51]
	v_mfma_f32_16x16x32_bf16 v[44:47], v[160:163], v[168:171], v[44:47]
	v_mfma_f32_16x16x32_bf16 v[32:35], v[152:155], v[176:179], v[32:35]
	v_mfma_f32_16x16x32_bf16 v[28:31], v[160:163], v[176:179], v[28:31]
	v_mfma_f32_16x16x32_bf16 v[16:19], v[152:155], v[184:187], v[16:19]
	v_mfma_f32_16x16x32_bf16 v[12:15], v[160:163], v[184:187], v[12:15]
	v_mfma_f32_16x16x32_bf16 v[8:11], v[152:155], v[192:195], v[8:11]
	v_mfma_f32_16x16x32_bf16 v[4:7], v[160:163], v[192:195], v[4:7]
	v_mfma_f32_16x16x32_bf16 v[48:51], v[156:159], v[172:175], v[48:51]
	v_mfma_f32_16x16x32_bf16 v[44:47], v[164:167], v[172:175], v[44:47]
	v_mfma_f32_16x16x32_bf16 v[32:35], v[156:159], v[180:183], v[32:35]
	v_mfma_f32_16x16x32_bf16 v[28:31], v[164:167], v[180:183], v[28:31]
	v_mfma_f32_16x16x32_bf16 v[16:19], v[156:159], v[188:191], v[16:19]
	v_mfma_f32_16x16x32_bf16 v[12:15], v[164:167], v[188:191], v[12:15]
	v_mfma_f32_16x16x32_bf16 v[8:11], v[156:159], v[196:199], v[8:11]
	v_mfma_f32_16x16x32_bf16 v[4:7], v[164:167], v[196:199], v[4:7]
	s_setprio 0
	s_barrier
	s_add_i32 s63, s63, 2
	s_add_u32 s61, s61, 0x10000
	s_addc_u32 s62, s62, 0
	s_add_u32 s12, s12, 0x100
	s_addc_u32 s13, s13, 0
	s_cmp_gt_u32 s63, 29
	s_cbranch_scc1 .LBB0_501

.LBB0_835:
	s_add_u32 s40, s14, 0x80
	s_addc_u32 s41, s15, 0
	s_waitcnt vmcnt(8)
	s_and_b64 s[38:39], s[38:39], exec
	s_waitcnt lgkmcnt(0)
	s_cselect_b32 s38, s13, s59
	s_cselect_b32 s43, s1, s41
	s_cselect_b32 s42, s0, s40
	s_cselect_b32 s39, s9, s60
	s_add_u32 s40, s38, 0x8000
	s_addc_u32 s41, s39, 0
	s_barrier
	s_setprio 1
	v_mfma_f32_16x16x32_bf16 v[132:135], v[152:155], v[192:195], v[132:135]
	v_mfma_f32_16x16x32_bf16 v[128:131], v[160:163], v[192:195], v[128:131]
	v_mfma_f32_16x16x32_bf16 v[124:127], v[152:155], v[184:187], v[124:127]
	v_mfma_f32_16x16x32_bf16 v[120:123], v[160:163], v[184:187], v[120:123]
	v_mfma_f32_16x16x32_bf16 v[108:111], v[152:155], v[176:179], v[108:111]
	v_mfma_f32_16x16x32_bf16 v[104:107], v[160:163], v[176:179], v[104:107]
	v_mfma_f32_16x16x32_bf16 v[92:95], v[152:155], v[168:171], v[92:95]
	v_mfma_f32_16x16x32_bf16 v[88:91], v[160:163], v[168:171], v[88:91]
	v_mfma_f32_16x16x32_bf16 v[132:135], v[156:159], v[196:199], v[132:135]
	v_mfma_f32_16x16x32_bf16 v[128:131], v[164:167], v[196:199], v[128:131]
	v_mfma_f32_16x16x32_bf16 v[124:127], v[156:159], v[188:191], v[124:127]
	v_mfma_f32_16x16x32_bf16 v[120:123], v[164:167], v[188:191], v[120:123]
	v_mfma_f32_16x16x32_bf16 v[108:111], v[156:159], v[180:183], v[108:111]
	v_mfma_f32_16x16x32_bf16 v[104:107], v[164:167], v[180:183], v[104:107]
	v_mfma_f32_16x16x32_bf16 v[92:95], v[156:159], v[172:175], v[92:95]
	v_mfma_f32_16x16x32_bf16 v[88:91], v[164:167], v[172:175], v[88:91]
	s_setprio 0
	s_setprio 1
	v_mfma_f32_16x16x32_bf16 v[116:119], v[136:139], v[192:195], v[116:119]
	v_mfma_f32_16x16x32_bf16 v[112:115], v[144:147], v[192:195], v[112:115]
	v_mfma_f32_16x16x32_bf16 v[100:103], v[136:139], v[184:187], v[100:103]
	v_mfma_f32_16x16x32_bf16 v[96:99], v[144:147], v[184:187], v[96:99]
	v_mfma_f32_16x16x32_bf16 v[80:83], v[136:139], v[176:179], v[80:83]
	v_mfma_f32_16x16x32_bf16 v[76:79], v[144:147], v[176:179], v[76:79]
	v_mfma_f32_16x16x32_bf16 v[72:75], v[136:139], v[168:171], v[72:75]
	v_mfma_f32_16x16x32_bf16 v[68:71], v[144:147], v[168:171], v[68:71]
	v_mfma_f32_16x16x32_bf16 v[116:119], v[140:143], v[196:199], v[116:119]
	v_mfma_f32_16x16x32_bf16 v[112:115], v[148:151], v[196:199], v[112:115]
	v_mfma_f32_16x16x32_bf16 v[100:103], v[140:143], v[188:191], v[100:103]
	v_mfma_f32_16x16x32_bf16 v[96:99], v[148:151], v[188:191], v[96:99]
	v_mfma_f32_16x16x32_bf16 v[80:83], v[140:143], v[180:183], v[80:83]
	v_mfma_f32_16x16x32_bf16 v[76:79], v[148:151], v[180:183], v[76:79]
	v_mfma_f32_16x16x32_bf16 v[72:75], v[140:143], v[172:175], v[72:75]
	v_mfma_f32_16x16x32_bf16 v[68:71], v[148:151], v[172:175], v[68:71]
	s_setprio 0
	s_barrier
	s_mov_b32 m0, s47
	v_lshl_add_u64 v[248:249], s[38:39], 0, v[210:211]
	s_add_u32 s62, s38, 0x4000
	ds_read_b128 v[168:171], v244 offset:16384
	ds_read_b128 v[172:175], v244 offset:17408
	ds_read_b128 v[176:179], v244 offset:18432
	ds_read_b128 v[180:183], v244 offset:19456
	ds_read_b128 v[184:187], v244 offset:20480
	ds_read_b128 v[188:191], v244 offset:21504
	ds_read_b128 v[192:195], v244 offset:22528
	ds_read_b128 v[196:199], v244 offset:23552
	global_load_lds_dwordx4 v[248:249], off
	v_lshl_add_u64 v[248:249], s[38:39], 0, v[208:209]
	s_mov_b32 m0, s48
	s_addc_u32 s63, s39, 0
	global_load_lds_dwordx4 v[248:249], off
	v_lshl_add_u64 v[248:249], s[62:63], 0, v[210:211]
	s_mov_b32 m0, s49
	v_mov_b32_e32 v215, v3
	global_load_lds_dwordx4 v[248:249], off
	v_lshl_add_u64 v[248:249], s[62:63], 0, v[208:209]
	s_mov_b32 m0, s50
	v_lshl_add_u64 v[204:205], s[42:43], 0, v[214:215]
	global_load_lds_dwordx4 v[248:249], off
	s_mov_b32 m0, s45
	v_lshl_add_u64 v[248:249], s[42:43], 0, v[2:3]
	global_load_lds_dwordx4 v2, s[42:43]
	s_mov_b32 m0, s51
	s_nop 0
	global_load_lds_dwordx4 v214, s[42:43]
	s_waitcnt vmcnt(8)
	s_waitcnt lgkmcnt(0)
	s_barrier
	s_setprio 1
	v_mfma_f32_16x16x32_bf16 v[64:67], v[152:155], v[168:171], v[64:67]
	v_mfma_f32_16x16x32_bf16 v[60:63], v[160:163], v[168:171], v[60:63]
	v_mfma_f32_16x16x32_bf16 v[56:59], v[152:155], v[176:179], v[56:59]
	v_mfma_f32_16x16x32_bf16 v[52:55], v[160:163], v[176:179], v[52:55]
	v_mfma_f32_16x16x32_bf16 v[40:43], v[152:155], v[184:187], v[40:43]
	v_mfma_f32_16x16x32_bf16 v[36:39], v[160:163], v[184:187], v[36:39]
	v_mfma_f32_16x16x32_bf16 v[24:27], v[152:155], v[192:195], v[24:27]
	v_mfma_f32_16x16x32_bf16 v[20:23], v[160:163], v[192:195], v[20:23]
	v_mfma_f32_16x16x32_bf16 v[64:67], v[156:159], v[172:175], v[64:67]
	v_mfma_f32_16x16x32_bf16 v[60:63], v[164:167], v[172:175], v[60:63]
	v_mfma_f32_16x16x32_bf16 v[56:59], v[156:159], v[180:183], v[56:59]
	v_mfma_f32_16x16x32_bf16 v[52:55], v[164:167], v[180:183], v[52:55]
	v_mfma_f32_16x16x32_bf16 v[40:43], v[156:159], v[188:191], v[40:43]
	v_mfma_f32_16x16x32_bf16 v[36:39], v[164:167], v[188:191], v[36:39]
	v_mfma_f32_16x16x32_bf16 v[24:27], v[156:159], v[196:199], v[24:27]
	v_mfma_f32_16x16x32_bf16 v[20:23], v[164:167], v[196:199], v[20:23]
	s_setprio 0
	s_setprio 1
	v_mfma_f32_16x16x32_bf16 v[48:51], v[136:139], v[168:171], v[48:51]
	v_mfma_f32_16x16x32_bf16 v[44:47], v[144:147], v[168:171], v[44:47]
	v_mfma_f32_16x16x32_bf16 v[32:35], v[136:139], v[176:179], v[32:35]
	v_mfma_f32_16x16x32_bf16 v[28:31], v[144:147], v[176:179], v[28:31]
	v_mfma_f32_16x16x32_bf16 v[16:19], v[136:139], v[184:187], v[16:19]
	v_mfma_f32_16x16x32_bf16 v[12:15], v[144:147], v[184:187], v[12:15]
	v_mfma_f32_16x16x32_bf16 v[8:11], v[136:139], v[192:195], v[8:11]
	v_mfma_f32_16x16x32_bf16 v[4:7], v[144:147], v[192:195], v[4:7]
	v_mfma_f32_16x16x32_bf16 v[48:51], v[140:143], v[172:175], v[48:51]
	v_mfma_f32_16x16x32_bf16 v[44:47], v[148:151], v[172:175], v[44:47]
	v_mfma_f32_16x16x32_bf16 v[32:35], v[140:143], v[180:183], v[32:35]
	v_mfma_f32_16x16x32_bf16 v[28:31], v[148:151], v[180:183], v[28:31]
	v_mfma_f32_16x16x32_bf16 v[16:19], v[140:143], v[188:191], v[16:19]
	v_mfma_f32_16x16x32_bf16 v[12:15], v[148:151], v[188:191], v[12:15]
	v_mfma_f32_16x16x32_bf16 v[8:11], v[140:143], v[196:199], v[8:11]
	v_mfma_f32_16x16x32_bf16 v[4:7], v[148:151], v[196:199], v[4:7]
	s_setprio 0
	s_barrier
	s_add_i32 s62, 0, 0x18000
	s_add_i32 s63, 0, 0x1c000
	v_add_u32_e32 v148, s62, v243
	v_add_u32_e32 v164, s63, v243
	ds_read_b128 v[136:139], v148
	ds_read_b128 v[140:143], v148 offset:1024
	ds_read_b128 v[144:147], v148 offset:2048
	ds_read_b128 v[148:151], v148 offset:3072
	ds_read_b128 v[152:155], v164
	ds_read_b128 v[156:159], v164 offset:1024
	ds_read_b128 v[160:163], v164 offset:2048
	ds_read_b128 v[164:167], v164 offset:3072
	s_mov_b32 m0, s52
	v_lshl_add_u64 v[226:227], s[42:43], 0, v[226:227]
	ds_read_b128 v[168:171], v244 offset:32768
	ds_read_b128 v[172:175], v244 offset:33792
	ds_read_b128 v[176:179], v244 offset:34816
	ds_read_b128 v[180:183], v244 offset:35840
	ds_read_b128 v[184:187], v244 offset:36864
	ds_read_b128 v[188:191], v244 offset:37888
	ds_read_b128 v[192:195], v244 offset:38912
	ds_read_b128 v[196:199], v244 offset:39936
	global_load_lds_dwordx4 v[226:227], off
	v_lshl_add_u64 v[224:225], s[42:43], 0, v[224:225]
	s_mov_b32 m0, s53
	s_nop 0
	global_load_lds_dwordx4 v[224:225], off
	s_waitcnt vmcnt(8)
	s_waitcnt lgkmcnt(0)
	s_barrier
	s_setprio 1
	v_mfma_f32_16x16x32_bf16 v[132:135], v[136:139], v[168:171], v[132:135]
	v_mfma_f32_16x16x32_bf16 v[128:131], v[144:147], v[168:171], v[128:131]
	v_mfma_f32_16x16x32_bf16 v[124:127], v[136:139], v[176:179], v[124:127]
	v_mfma_f32_16x16x32_bf16 v[120:123], v[144:147], v[176:179], v[120:123]
	v_mfma_f32_16x16x32_bf16 v[108:111], v[136:139], v[184:187], v[108:111]
	v_mfma_f32_16x16x32_bf16 v[104:107], v[144:147], v[184:187], v[104:107]
	v_mfma_f32_16x16x32_bf16 v[92:95], v[136:139], v[192:195], v[92:95]
	v_mfma_f32_16x16x32_bf16 v[88:91], v[144:147], v[192:195], v[88:91]
	v_mfma_f32_16x16x32_bf16 v[132:135], v[140:143], v[172:175], v[132:135]
	v_mfma_f32_16x16x32_bf16 v[128:131], v[148:151], v[172:175], v[128:131]
	v_mfma_f32_16x16x32_bf16 v[124:127], v[140:143], v[180:183], v[124:127]
	v_mfma_f32_16x16x32_bf16 v[120:123], v[148:151], v[180:183], v[120:123]
	v_mfma_f32_16x16x32_bf16 v[108:111], v[140:143], v[188:191], v[108:111]
	v_mfma_f32_16x16x32_bf16 v[104:107], v[148:151], v[188:191], v[104:107]
	v_mfma_f32_16x16x32_bf16 v[92:95], v[140:143], v[196:199], v[92:95]
	v_mfma_f32_16x16x32_bf16 v[88:91], v[148:151], v[196:199], v[88:91]
	s_setprio 0
	s_setprio 1
	v_mfma_f32_16x16x32_bf16 v[116:119], v[152:155], v[168:171], v[116:119]
	v_mfma_f32_16x16x32_bf16 v[112:115], v[160:163], v[168:171], v[112:115]
	v_mfma_f32_16x16x32_bf16 v[100:103], v[152:155], v[176:179], v[100:103]
	v_mfma_f32_16x16x32_bf16 v[96:99], v[160:163], v[176:179], v[96:99]
	v_mfma_f32_16x16x32_bf16 v[80:83], v[152:155], v[184:187], v[80:83]
	v_mfma_f32_16x16x32_bf16 v[76:79], v[160:163], v[184:187], v[76:79]
	v_mfma_f32_16x16x32_bf16 v[72:75], v[152:155], v[192:195], v[72:75]
	v_mfma_f32_16x16x32_bf16 v[68:71], v[160:163], v[192:195], v[68:71]
	v_mfma_f32_16x16x32_bf16 v[116:119], v[156:159], v[172:175], v[116:119]
	v_mfma_f32_16x16x32_bf16 v[112:115], v[164:167], v[172:175], v[112:115]
	v_mfma_f32_16x16x32_bf16 v[100:103], v[156:159], v[180:183], v[100:103]
	v_mfma_f32_16x16x32_bf16 v[96:99], v[164:167], v[180:183], v[96:99]
	v_mfma_f32_16x16x32_bf16 v[80:83], v[156:159], v[188:191], v[80:83]
	v_mfma_f32_16x16x32_bf16 v[76:79], v[164:167], v[188:191], v[76:79]
	v_mfma_f32_16x16x32_bf16 v[72:75], v[156:159], v[196:199], v[72:75]
	v_mfma_f32_16x16x32_bf16 v[68:71], v[164:167], v[196:199], v[68:71]
	s_setprio 0
	s_barrier
	s_add_i32 s42, s62, s44
	v_lshl_add_u64 v[224:225], s[40:41], 0, v[210:211]
	s_mov_b32 m0, s42
	ds_read_b128 v[168:171], v244 offset:49152
	ds_read_b128 v[172:175], v244 offset:50176
	ds_read_b128 v[176:179], v244 offset:51200
	ds_read_b128 v[180:183], v244 offset:52224
	ds_read_b128 v[184:187], v244 offset:53248
	ds_read_b128 v[188:191], v244 offset:54272
	ds_read_b128 v[192:195], v244 offset:55296
	ds_read_b128 v[196:199], v244 offset:56320
	global_load_lds_dwordx4 v[224:225], off
	s_add_i32 m0, s42, 0x2000
	s_add_u32 s38, s38, 0xc000
	v_lshl_add_u64 v[224:225], s[40:41], 0, v[208:209]
	s_addc_u32 s39, s39, 0
	s_add_i32 s40, s63, s44
	global_load_lds_dwordx4 v[224:225], off
	v_lshl_add_u64 v[224:225], s[38:39], 0, v[210:211]
	s_mov_b32 m0, s40
	v_lshl_add_u64 v[204:205], v[204:205], 0, s[36:37]
	global_load_lds_dwordx4 v[224:225], off
	v_lshl_add_u64 v[224:225], s[38:39], 0, v[208:209]
	s_add_i32 m0, s40, 0x2000
	s_nop 0
	global_load_lds_dwordx4 v[224:225], off
	v_lshl_add_u64 v[224:225], v[248:249], 0, s[36:37]
	s_mov_b32 m0, s54
	s_nop 0
	global_load_lds_dwordx4 v[224:225], off
	s_mov_b32 m0, s55
	s_nop 0
	global_load_lds_dwordx4 v[204:205], off
	s_waitcnt vmcnt(8)
	s_waitcnt lgkmcnt(0)
	s_barrier
	s_setprio 1
	v_mfma_f32_16x16x32_bf16 v[64:67], v[136:139], v[168:171], v[64:67]
	v_mfma_f32_16x16x32_bf16 v[60:63], v[144:147], v[168:171], v[60:63]
	v_mfma_f32_16x16x32_bf16 v[56:59], v[136:139], v[176:179], v[56:59]
	v_mfma_f32_16x16x32_bf16 v[52:55], v[144:147], v[176:179], v[52:55]
	v_mfma_f32_16x16x32_bf16 v[40:43], v[136:139], v[184:187], v[40:43]
	v_mfma_f32_16x16x32_bf16 v[36:39], v[144:147], v[184:187], v[36:39]
	v_mfma_f32_16x16x32_bf16 v[24:27], v[136:139], v[192:195], v[24:27]
	v_mfma_f32_16x16x32_bf16 v[20:23], v[144:147], v[192:195], v[20:23]
	v_mfma_f32_16x16x32_bf16 v[64:67], v[140:143], v[172:175], v[64:67]
	v_mfma_f32_16x16x32_bf16 v[60:63], v[148:151], v[172:175], v[60:63]
	v_mfma_f32_16x16x32_bf16 v[56:59], v[140:143], v[180:183], v[56:59]
	v_mfma_f32_16x16x32_bf16 v[52:55], v[148:151], v[180:183], v[52:55]
	v_mfma_f32_16x16x32_bf16 v[40:43], v[140:143], v[188:191], v[40:43]
	v_mfma_f32_16x16x32_bf16 v[36:39], v[148:151], v[188:191], v[36:39]
	v_mfma_f32_16x16x32_bf16 v[24:27], v[140:143], v[196:199], v[24:27]
	v_mfma_f32_16x16x32_bf16 v[20:23], v[148:151], v[196:199], v[20:23]
	s_setprio 0
	s_setprio 1
	v_mfma_f32_16x16x32_bf16 v[48:51], v[152:155], v[168:171], v[48:51]
	v_mfma_f32_16x16x32_bf16 v[44:47], v[160:163], v[168:171], v[44:47]
	v_mfma_f32_16x16x32_bf16 v[32:35], v[152:155], v[176:179], v[32:35]
	v_mfma_f32_16x16x32_bf16 v[28:31], v[160:163], v[176:179], v[28:31]
	v_mfma_f32_16x16x32_bf16 v[16:19], v[152:155], v[184:187], v[16:19]
	v_mfma_f32_16x16x32_bf16 v[12:15], v[160:163], v[184:187], v[12:15]
	v_mfma_f32_16x16x32_bf16 v[8:11], v[152:155], v[192:195], v[8:11]
	v_mfma_f32_16x16x32_bf16 v[4:7], v[160:163], v[192:195], v[4:7]
	v_mfma_f32_16x16x32_bf16 v[48:51], v[156:159], v[172:175], v[48:51]
	v_mfma_f32_16x16x32_bf16 v[44:47], v[164:167], v[172:175], v[44:47]
	v_mfma_f32_16x16x32_bf16 v[32:35], v[156:159], v[180:183], v[32:35]
	v_mfma_f32_16x16x32_bf16 v[28:31], v[164:167], v[180:183], v[28:31]
	v_mfma_f32_16x16x32_bf16 v[16:19], v[156:159], v[188:191], v[16:19]
	v_mfma_f32_16x16x32_bf16 v[12:15], v[164:167], v[188:191], v[12:15]
	v_mfma_f32_16x16x32_bf16 v[8:11], v[156:159], v[196:199], v[8:11]
	v_mfma_f32_16x16x32_bf16 v[4:7], v[164:167], v[196:199], v[4:7]
	s_setprio 0
	s_barrier
	s_add_i32 s61, s61, 2
	s_add_u32 s59, s59, 0x10000
	s_addc_u32 s60, s60, 0
	s_add_u32 s14, s14, 0x100
	s_addc_u32 s15, s15, 0
	s_cmp_gt_u32 s61, 29
	s_cbranch_scc1 .LBB0_838

.LBB0_1175:
	s_waitcnt vmcnt(8)
	s_waitcnt lgkmcnt(0)
	s_barrier
	s_setprio 1
	v_mfma_f32_16x16x32_bf16 v[132:135], v[152:155], v[180:183], v[132:135]
	v_mfma_f32_16x16x32_bf16 v[128:131], v[160:163], v[180:183], v[128:131]
	v_mfma_f32_16x16x32_bf16 v[124:127], v[152:155], v[176:179], v[124:127]
	v_mfma_f32_16x16x32_bf16 v[120:123], v[160:163], v[176:179], v[120:123]
	v_mfma_f32_16x16x32_bf16 v[116:119], v[152:155], v[172:175], v[116:119]
	v_mfma_f32_16x16x32_bf16 v[112:115], v[160:163], v[172:175], v[112:115]
	v_mfma_f32_16x16x32_bf16 v[108:111], v[152:155], v[168:171], v[108:111]
	v_mfma_f32_16x16x32_bf16 v[104:107], v[160:163], v[168:171], v[104:107]
	v_mfma_f32_16x16x32_bf16 v[132:135], v[156:159], v[196:199], v[132:135]
	v_mfma_f32_16x16x32_bf16 v[128:131], v[164:167], v[196:199], v[128:131]
	v_mfma_f32_16x16x32_bf16 v[124:127], v[156:159], v[192:195], v[124:127]
	v_mfma_f32_16x16x32_bf16 v[120:123], v[164:167], v[192:195], v[120:123]
	v_mfma_f32_16x16x32_bf16 v[116:119], v[156:159], v[188:191], v[116:119]
	v_mfma_f32_16x16x32_bf16 v[112:115], v[164:167], v[188:191], v[112:115]
	v_mfma_f32_16x16x32_bf16 v[108:111], v[156:159], v[184:187], v[108:111]
	v_mfma_f32_16x16x32_bf16 v[104:107], v[164:167], v[184:187], v[104:107]
	s_setprio 0
	s_setprio 1
	v_mfma_f32_16x16x32_bf16 v[100:103], v[136:139], v[180:183], v[100:103]
	v_mfma_f32_16x16x32_bf16 v[96:99], v[144:147], v[180:183], v[96:99]
	v_mfma_f32_16x16x32_bf16 v[92:95], v[136:139], v[176:179], v[92:95]
	v_mfma_f32_16x16x32_bf16 v[88:91], v[144:147], v[176:179], v[88:91]
	v_mfma_f32_16x16x32_bf16 v[80:83], v[136:139], v[172:175], v[80:83]
	v_mfma_f32_16x16x32_bf16 v[76:79], v[144:147], v[172:175], v[76:79]
	v_mfma_f32_16x16x32_bf16 v[72:75], v[136:139], v[168:171], v[72:75]
	v_mfma_f32_16x16x32_bf16 v[68:71], v[144:147], v[168:171], v[68:71]
	v_mfma_f32_16x16x32_bf16 v[100:103], v[140:143], v[196:199], v[100:103]
	v_mfma_f32_16x16x32_bf16 v[96:99], v[148:151], v[196:199], v[96:99]
	v_mfma_f32_16x16x32_bf16 v[92:95], v[140:143], v[192:195], v[92:95]
	v_mfma_f32_16x16x32_bf16 v[88:91], v[148:151], v[192:195], v[88:91]
	v_mfma_f32_16x16x32_bf16 v[80:83], v[140:143], v[188:191], v[80:83]
	v_mfma_f32_16x16x32_bf16 v[76:79], v[148:151], v[188:191], v[76:79]
	v_mfma_f32_16x16x32_bf16 v[72:75], v[140:143], v[184:187], v[72:75]
	v_mfma_f32_16x16x32_bf16 v[68:71], v[148:151], v[184:187], v[68:71]
	s_setprio 0
	s_barrier
	v_cndmask_b32_e64 v200, 0, 1, s[2:3]
	v_cmp_ne_u32_e64 s[4:5], 1, v200
	s_andn2_b64 vcc, exec, s[2:3]
	s_cbranch_vccnz .LBB0_1177
	ds_read_b128 v[180:183], v225 offset:16384
	ds_read_b128 v[196:199], v225 offset:17408
	ds_read_b128 v[176:179], v225 offset:18432
	ds_read_b128 v[192:195], v225 offset:19456
	ds_read_b128 v[172:175], v225 offset:20480
	ds_read_b128 v[188:191], v225 offset:21504
	ds_read_b128 v[168:171], v225 offset:22528
	ds_read_b128 v[184:187], v225 offset:23552
.LBB0_1177:
	s_add_u32 s56, s52, 0x80
	s_addc_u32 s57, s53, 0
	s_and_b64 s[54:55], s[54:55], exec
	s_cselect_b32 s55, s11, s81
	s_cselect_b32 s54, s41, s80
	s_mov_b32 m0, s61
	s_cselect_b32 s57, s23, s57
	s_cselect_b32 s56, s22, s56
	v_lshl_add_u64 v[204:205], s[54:55], 0, v[208:209]
	s_add_u32 s84, s54, 0x4000
	global_load_lds_dwordx4 v[204:205], off
	v_lshl_add_u64 v[204:205], s[54:55], 0, v[210:211]
	s_mov_b32 m0, s62
	s_addc_u32 s85, s55, 0
	global_load_lds_dwordx4 v[204:205], off
	v_lshl_add_u64 v[204:205], s[84:85], 0, v[208:209]
	s_mov_b32 m0, s63
	s_and_b64 vcc, exec, s[4:5]
	global_load_lds_dwordx4 v[204:205], off
	v_lshl_add_u64 v[204:205], s[84:85], 0, v[210:211]
	s_mov_b32 m0, s64
	s_nop 0
	global_load_lds_dwordx4 v[204:205], off
	s_mov_b32 m0, s9
	s_nop 0
	global_load_lds_dwordx4 v2, s[56:57]
	s_mov_b32 m0, s65
	s_nop 0
	global_load_lds_dwordx4 v212, s[56:57]
	s_waitcnt vmcnt(8)
	s_waitcnt lgkmcnt(0)
	s_barrier
	s_cbranch_vccnz .LBB0_1179
	s_setprio 1
	v_mfma_f32_16x16x32_bf16 v[64:67], v[152:155], v[180:183], v[64:67]
	v_mfma_f32_16x16x32_bf16 v[60:63], v[160:163], v[180:183], v[60:63]
	v_mfma_f32_16x16x32_bf16 v[56:59], v[152:155], v[176:179], v[56:59]
	v_mfma_f32_16x16x32_bf16 v[52:55], v[160:163], v[176:179], v[52:55]
	v_mfma_f32_16x16x32_bf16 v[48:51], v[152:155], v[172:175], v[48:51]
	v_mfma_f32_16x16x32_bf16 v[44:47], v[160:163], v[172:175], v[44:47]
	v_mfma_f32_16x16x32_bf16 v[40:43], v[152:155], v[168:171], v[40:43]
	v_mfma_f32_16x16x32_bf16 v[36:39], v[160:163], v[168:171], v[36:39]
	v_mfma_f32_16x16x32_bf16 v[64:67], v[156:159], v[196:199], v[64:67]
	v_mfma_f32_16x16x32_bf16 v[60:63], v[164:167], v[196:199], v[60:63]
	v_mfma_f32_16x16x32_bf16 v[56:59], v[156:159], v[192:195], v[56:59]
	v_mfma_f32_16x16x32_bf16 v[52:55], v[164:167], v[192:195], v[52:55]
	v_mfma_f32_16x16x32_bf16 v[48:51], v[156:159], v[188:191], v[48:51]
	v_mfma_f32_16x16x32_bf16 v[44:47], v[164:167], v[188:191], v[44:47]
	v_mfma_f32_16x16x32_bf16 v[40:43], v[156:159], v[184:187], v[40:43]
	v_mfma_f32_16x16x32_bf16 v[36:39], v[164:167], v[184:187], v[36:39]
	s_setprio 0
	s_setprio 1
	v_mfma_f32_16x16x32_bf16 v[32:35], v[136:139], v[180:183], v[32:35]
	v_mfma_f32_16x16x32_bf16 v[28:31], v[144:147], v[180:183], v[28:31]
	v_mfma_f32_16x16x32_bf16 v[24:27], v[136:139], v[176:179], v[24:27]
	v_mfma_f32_16x16x32_bf16 v[20:23], v[144:147], v[176:179], v[20:23]
	v_mfma_f32_16x16x32_bf16 v[16:19], v[136:139], v[172:175], v[16:19]
	v_mfma_f32_16x16x32_bf16 v[12:15], v[144:147], v[172:175], v[12:15]
	v_mfma_f32_16x16x32_bf16 v[8:11], v[136:139], v[168:171], v[8:11]
	v_mfma_f32_16x16x32_bf16 v[4:7], v[144:147], v[168:171], v[4:7]
	v_mfma_f32_16x16x32_bf16 v[32:35], v[140:143], v[196:199], v[32:35]
	v_mfma_f32_16x16x32_bf16 v[28:31], v[148:151], v[196:199], v[28:31]
	v_mfma_f32_16x16x32_bf16 v[24:27], v[140:143], v[192:195], v[24:27]
	v_mfma_f32_16x16x32_bf16 v[20:23], v[148:151], v[192:195], v[20:23]
	v_mfma_f32_16x16x32_bf16 v[16:19], v[140:143], v[188:191], v[16:19]
	v_mfma_f32_16x16x32_bf16 v[12:15], v[148:151], v[188:191], v[12:15]
	v_mfma_f32_16x16x32_bf16 v[8:11], v[140:143], v[184:187], v[8:11]
	v_mfma_f32_16x16x32_bf16 v[4:7], v[148:151], v[184:187], v[4:7]
	s_setprio 0
.LBB0_1179:
	s_barrier
	v_add_u32_e32 v136, 0x18000, v224
	v_add_u32_e32 v148, 0x1c000, v224
	ds_read_b128 v[152:155], v136
	ds_read_b128 v[156:159], v136 offset:1024
	ds_read_b128 v[160:163], v136 offset:2048
	ds_read_b128 v[164:167], v136 offset:3072
	ds_read_b128 v[136:139], v148
	ds_read_b128 v[140:143], v148 offset:1024
	ds_read_b128 v[144:147], v148 offset:2048
	ds_read_b128 v[148:151], v148 offset:3072
	s_mov_b32 m0, s66
	s_waitcnt lgkmcnt(0)
	ds_read_b128 v[180:183], v225 offset:32768
	ds_read_b128 v[196:199], v225 offset:33792
	ds_read_b128 v[176:179], v225 offset:34816
	ds_read_b128 v[192:195], v225 offset:35840
	ds_read_b128 v[172:175], v225 offset:36864
	ds_read_b128 v[188:191], v225 offset:37888
	ds_read_b128 v[168:171], v225 offset:38912
	ds_read_b128 v[184:187], v225 offset:39936
	global_load_lds_dwordx4 v218, s[56:57]
	s_mov_b32 m0, s67
	s_nop 0
	global_load_lds_dwordx4 v220, s[56:57]
	s_waitcnt vmcnt(8)
	s_waitcnt lgkmcnt(0)
	s_barrier
	s_setprio 1
	v_mfma_f32_16x16x32_bf16 v[132:135], v[152:155], v[180:183], v[132:135]
	v_mfma_f32_16x16x32_bf16 v[128:131], v[160:163], v[180:183], v[128:131]
	v_mfma_f32_16x16x32_bf16 v[124:127], v[152:155], v[176:179], v[124:127]
	v_mfma_f32_16x16x32_bf16 v[120:123], v[160:163], v[176:179], v[120:123]
	v_mfma_f32_16x16x32_bf16 v[116:119], v[152:155], v[172:175], v[116:119]
	v_mfma_f32_16x16x32_bf16 v[112:115], v[160:163], v[172:175], v[112:115]
	v_mfma_f32_16x16x32_bf16 v[108:111], v[152:155], v[168:171], v[108:111]
	v_mfma_f32_16x16x32_bf16 v[104:107], v[160:163], v[168:171], v[104:107]
	v_mfma_f32_16x16x32_bf16 v[132:135], v[156:159], v[196:199], v[132:135]
	v_mfma_f32_16x16x32_bf16 v[128:131], v[164:167], v[196:199], v[128:131]
	v_mfma_f32_16x16x32_bf16 v[124:127], v[156:159], v[192:195], v[124:127]
	v_mfma_f32_16x16x32_bf16 v[120:123], v[164:167], v[192:195], v[120:123]
	v_mfma_f32_16x16x32_bf16 v[116:119], v[156:159], v[188:191], v[116:119]
	v_mfma_f32_16x16x32_bf16 v[112:115], v[164:167], v[188:191], v[112:115]
	v_mfma_f32_16x16x32_bf16 v[108:111], v[156:159], v[184:187], v[108:111]
	v_mfma_f32_16x16x32_bf16 v[104:107], v[164:167], v[184:187], v[104:107]
	s_setprio 0
	s_setprio 1
	v_mfma_f32_16x16x32_bf16 v[100:103], v[136:139], v[180:183], v[100:103]
	v_mfma_f32_16x16x32_bf16 v[96:99], v[144:147], v[180:183], v[96:99]
	v_mfma_f32_16x16x32_bf16 v[92:95], v[136:139], v[176:179], v[92:95]
	v_mfma_f32_16x16x32_bf16 v[88:91], v[144:147], v[176:179], v[88:91]
	v_mfma_f32_16x16x32_bf16 v[80:83], v[136:139], v[172:175], v[80:83]
	v_mfma_f32_16x16x32_bf16 v[76:79], v[144:147], v[172:175], v[76:79]
	v_mfma_f32_16x16x32_bf16 v[72:75], v[136:139], v[168:171], v[72:75]
	v_mfma_f32_16x16x32_bf16 v[68:71], v[144:147], v[168:171], v[68:71]
	v_mfma_f32_16x16x32_bf16 v[100:103], v[140:143], v[196:199], v[100:103]
	v_mfma_f32_16x16x32_bf16 v[96:99], v[148:151], v[196:199], v[96:99]
	v_mfma_f32_16x16x32_bf16 v[92:95], v[140:143], v[192:195], v[92:95]
	v_mfma_f32_16x16x32_bf16 v[88:91], v[148:151], v[192:195], v[88:91]
	v_mfma_f32_16x16x32_bf16 v[80:83], v[140:143], v[188:191], v[80:83]
	v_mfma_f32_16x16x32_bf16 v[76:79], v[148:151], v[188:191], v[76:79]
	v_mfma_f32_16x16x32_bf16 v[72:75], v[140:143], v[184:187], v[72:75]
	v_mfma_f32_16x16x32_bf16 v[68:71], v[148:151], v[184:187], v[68:71]
	s_setprio 0
	s_barrier
	s_and_b64 vcc, exec, s[4:5]
	s_cbranch_vccnz .LBB0_1181
	ds_read_b128 v[180:183], v225 offset:49152
	ds_read_b128 v[196:199], v225 offset:50176
	ds_read_b128 v[176:179], v225 offset:51200
	ds_read_b128 v[192:195], v225 offset:52224
	ds_read_b128 v[172:175], v225 offset:53248
	ds_read_b128 v[188:191], v225 offset:54272
	ds_read_b128 v[168:171], v225 offset:55296
	ds_read_b128 v[184:187], v225 offset:56320
.LBB0_1181:
	v_mov_b32_e32 v213, v3
	v_lshl_add_u64 v[204:205], s[56:57], 0, v[2:3]
	v_lshl_add_u64 v[240:241], s[56:57], 0, v[212:213]
	s_add_u32 s56, s54, 0x8000
	s_addc_u32 s57, s55, 0
	s_mov_b32 m0, s69
	v_lshl_add_u64 v[242:243], s[56:57], 0, v[208:209]
	s_add_u32 s54, s54, 0xc000
	global_load_lds_dwordx4 v[242:243], off
	v_lshl_add_u64 v[242:243], s[56:57], 0, v[210:211]
	s_mov_b32 m0, s70
	s_addc_u32 s55, s55, 0
	global_load_lds_dwordx4 v[242:243], off
	v_lshl_add_u64 v[242:243], s[54:55], 0, v[208:209]
	s_mov_b32 m0, s73
	v_lshl_add_u64 v[204:205], v[204:205], 0, s[36:37]
	global_load_lds_dwordx4 v[242:243], off
	v_lshl_add_u64 v[242:243], s[54:55], 0, v[210:211]
	s_mov_b32 m0, s74
	s_and_b64 vcc, exec, s[4:5]
	global_load_lds_dwordx4 v[242:243], off
	s_mov_b32 m0, s71
	s_nop 0
	global_load_lds_dwordx4 v[204:205], off
	v_lshl_add_u64 v[204:205], v[240:241], 0, s[36:37]
	s_mov_b32 m0, s72
	s_nop 0
	global_load_lds_dwordx4 v[204:205], off
	s_waitcnt vmcnt(8)
	s_waitcnt lgkmcnt(0)
	s_barrier
	s_cbranch_vccnz .LBB0_1164
	s_setprio 1
	v_mfma_f32_16x16x32_bf16 v[64:67], v[152:155], v[180:183], v[64:67]
	v_mfma_f32_16x16x32_bf16 v[60:63], v[160:163], v[180:183], v[60:63]
	v_mfma_f32_16x16x32_bf16 v[56:59], v[152:155], v[176:179], v[56:59]
	v_mfma_f32_16x16x32_bf16 v[52:55], v[160:163], v[176:179], v[52:55]
	v_mfma_f32_16x16x32_bf16 v[48:51], v[152:155], v[172:175], v[48:51]
	v_mfma_f32_16x16x32_bf16 v[44:47], v[160:163], v[172:175], v[44:47]
	v_mfma_f32_16x16x32_bf16 v[40:43], v[152:155], v[168:171], v[40:43]
	v_mfma_f32_16x16x32_bf16 v[36:39], v[160:163], v[168:171], v[36:39]
	v_mfma_f32_16x16x32_bf16 v[64:67], v[156:159], v[196:199], v[64:67]
	v_mfma_f32_16x16x32_bf16 v[60:63], v[164:167], v[196:199], v[60:63]
	v_mfma_f32_16x16x32_bf16 v[56:59], v[156:159], v[192:195], v[56:59]
	v_mfma_f32_16x16x32_bf16 v[52:55], v[164:167], v[192:195], v[52:55]
	v_mfma_f32_16x16x32_bf16 v[48:51], v[156:159], v[188:191], v[48:51]
	v_mfma_f32_16x16x32_bf16 v[44:47], v[164:167], v[188:191], v[44:47]
	v_mfma_f32_16x16x32_bf16 v[40:43], v[156:159], v[184:187], v[40:43]
	v_mfma_f32_16x16x32_bf16 v[36:39], v[164:167], v[184:187], v[36:39]
	s_setprio 0
	s_setprio 1
	v_mfma_f32_16x16x32_bf16 v[32:35], v[136:139], v[180:183], v[32:35]
	v_mfma_f32_16x16x32_bf16 v[28:31], v[144:147], v[180:183], v[28:31]
	v_mfma_f32_16x16x32_bf16 v[24:27], v[136:139], v[176:179], v[24:27]
	v_mfma_f32_16x16x32_bf16 v[20:23], v[144:147], v[176:179], v[20:23]
	v_mfma_f32_16x16x32_bf16 v[16:19], v[136:139], v[172:175], v[16:19]
	v_mfma_f32_16x16x32_bf16 v[12:15], v[144:147], v[172:175], v[12:15]
	v_mfma_f32_16x16x32_bf16 v[8:11], v[136:139], v[168:171], v[8:11]
	v_mfma_f32_16x16x32_bf16 v[4:7], v[144:147], v[168:171], v[4:7]
	v_mfma_f32_16x16x32_bf16 v[32:35], v[140:143], v[196:199], v[32:35]
	v_mfma_f32_16x16x32_bf16 v[28:31], v[148:151], v[196:199], v[28:31]
	v_mfma_f32_16x16x32_bf16 v[24:27], v[140:143], v[192:195], v[24:27]
	v_mfma_f32_16x16x32_bf16 v[20:23], v[148:151], v[192:195], v[20:23]
	v_mfma_f32_16x16x32_bf16 v[16:19], v[140:143], v[188:191], v[16:19]
	v_mfma_f32_16x16x32_bf16 v[12:15], v[148:151], v[188:191], v[12:15]
	v_mfma_f32_16x16x32_bf16 v[8:11], v[140:143], v[184:187], v[8:11]
	v_mfma_f32_16x16x32_bf16 v[4:7], v[148:151], v[184:187], v[4:7]
	s_setprio 0
	s_branch .LBB0_1164

.LBB0_1311:
	s_waitcnt vmcnt(8)
	s_waitcnt lgkmcnt(0)
	s_barrier
	s_setprio 1
	v_mfma_f32_16x16x32_bf16 v[132:135], v[152:155], v[180:183], v[132:135]
	v_mfma_f32_16x16x32_bf16 v[128:131], v[160:163], v[180:183], v[128:131]
	v_mfma_f32_16x16x32_bf16 v[124:127], v[152:155], v[176:179], v[124:127]
	v_mfma_f32_16x16x32_bf16 v[120:123], v[160:163], v[176:179], v[120:123]
	v_mfma_f32_16x16x32_bf16 v[116:119], v[152:155], v[172:175], v[116:119]
	v_mfma_f32_16x16x32_bf16 v[112:115], v[160:163], v[172:175], v[112:115]
	v_mfma_f32_16x16x32_bf16 v[108:111], v[152:155], v[168:171], v[108:111]
	v_mfma_f32_16x16x32_bf16 v[104:107], v[160:163], v[168:171], v[104:107]
	v_mfma_f32_16x16x32_bf16 v[132:135], v[156:159], v[196:199], v[132:135]
	v_mfma_f32_16x16x32_bf16 v[128:131], v[164:167], v[196:199], v[128:131]
	v_mfma_f32_16x16x32_bf16 v[124:127], v[156:159], v[192:195], v[124:127]
	v_mfma_f32_16x16x32_bf16 v[120:123], v[164:167], v[192:195], v[120:123]
	v_mfma_f32_16x16x32_bf16 v[116:119], v[156:159], v[188:191], v[116:119]
	v_mfma_f32_16x16x32_bf16 v[112:115], v[164:167], v[188:191], v[112:115]
	v_mfma_f32_16x16x32_bf16 v[108:111], v[156:159], v[184:187], v[108:111]
	v_mfma_f32_16x16x32_bf16 v[104:107], v[164:167], v[184:187], v[104:107]
	s_setprio 0
	s_setprio 1
	v_mfma_f32_16x16x32_bf16 v[100:103], v[136:139], v[180:183], v[100:103]
	v_mfma_f32_16x16x32_bf16 v[96:99], v[144:147], v[180:183], v[96:99]
	v_mfma_f32_16x16x32_bf16 v[92:95], v[136:139], v[176:179], v[92:95]
	v_mfma_f32_16x16x32_bf16 v[88:91], v[144:147], v[176:179], v[88:91]
	v_mfma_f32_16x16x32_bf16 v[80:83], v[136:139], v[172:175], v[80:83]
	v_mfma_f32_16x16x32_bf16 v[76:79], v[144:147], v[172:175], v[76:79]
	v_mfma_f32_16x16x32_bf16 v[72:75], v[136:139], v[168:171], v[72:75]
	v_mfma_f32_16x16x32_bf16 v[68:71], v[144:147], v[168:171], v[68:71]
	v_mfma_f32_16x16x32_bf16 v[100:103], v[140:143], v[196:199], v[100:103]
	v_mfma_f32_16x16x32_bf16 v[96:99], v[148:151], v[196:199], v[96:99]
	v_mfma_f32_16x16x32_bf16 v[92:95], v[140:143], v[192:195], v[92:95]
	v_mfma_f32_16x16x32_bf16 v[88:91], v[148:151], v[192:195], v[88:91]
	v_mfma_f32_16x16x32_bf16 v[80:83], v[140:143], v[188:191], v[80:83]
	v_mfma_f32_16x16x32_bf16 v[76:79], v[148:151], v[188:191], v[76:79]
	v_mfma_f32_16x16x32_bf16 v[72:75], v[140:143], v[184:187], v[72:75]
	v_mfma_f32_16x16x32_bf16 v[68:71], v[148:151], v[184:187], v[68:71]
	s_setprio 0
	s_barrier
	v_cndmask_b32_e64 v200, 0, 1, s[2:3]
	v_cmp_ne_u32_e64 s[4:5], 1, v200
	s_andn2_b64 vcc, exec, s[2:3]
	s_cbranch_vccnz .LBB0_1313
	ds_read_b128 v[180:183], v242 offset:16384
	ds_read_b128 v[196:199], v242 offset:17408
	ds_read_b128 v[176:179], v242 offset:18432
	ds_read_b128 v[192:195], v242 offset:19456
	ds_read_b128 v[172:175], v242 offset:20480
	ds_read_b128 v[188:191], v242 offset:21504
	ds_read_b128 v[168:171], v242 offset:22528
	ds_read_b128 v[184:187], v242 offset:23552
.LBB0_1313:
	s_add_u32 s56, s52, 0x80
	s_addc_u32 s57, s53, 0
	s_and_b64 s[54:55], s[54:55], exec
	s_cselect_b32 s55, s41, s83
	s_cselect_b32 s54, s43, s82
	s_mov_b32 m0, s65
	s_cselect_b32 s57, s25, s57
	s_cselect_b32 s56, s24, s56
	v_lshl_add_u64 v[204:205], s[54:55], 0, v[208:209]
	s_add_u32 s86, s54, 0x4000
	global_load_lds_dwordx4 v[204:205], off
	v_lshl_add_u64 v[204:205], s[54:55], 0, v[210:211]
	s_mov_b32 m0, s66
	s_addc_u32 s87, s55, 0
	global_load_lds_dwordx4 v[204:205], off
	v_lshl_add_u64 v[204:205], s[86:87], 0, v[208:209]
	s_mov_b32 m0, s67
	s_and_b64 vcc, exec, s[4:5]
	global_load_lds_dwordx4 v[204:205], off
	v_lshl_add_u64 v[204:205], s[86:87], 0, v[210:211]
	s_mov_b32 m0, s68
	s_nop 0
	global_load_lds_dwordx4 v[204:205], off
	s_mov_b32 m0, s11
	s_nop 0
	global_load_lds_dwordx4 v2, s[56:57]
	s_mov_b32 m0, s69
	s_nop 0
	global_load_lds_dwordx4 v212, s[56:57]
	s_waitcnt vmcnt(8)
	s_waitcnt lgkmcnt(0)
	s_barrier
	s_cbranch_vccnz .LBB0_1315
	s_setprio 1
	v_mfma_f32_16x16x32_bf16 v[64:67], v[152:155], v[180:183], v[64:67]
	v_mfma_f32_16x16x32_bf16 v[60:63], v[160:163], v[180:183], v[60:63]
	v_mfma_f32_16x16x32_bf16 v[56:59], v[152:155], v[176:179], v[56:59]
	v_mfma_f32_16x16x32_bf16 v[52:55], v[160:163], v[176:179], v[52:55]
	v_mfma_f32_16x16x32_bf16 v[48:51], v[152:155], v[172:175], v[48:51]
	v_mfma_f32_16x16x32_bf16 v[44:47], v[160:163], v[172:175], v[44:47]
	v_mfma_f32_16x16x32_bf16 v[40:43], v[152:155], v[168:171], v[40:43]
	v_mfma_f32_16x16x32_bf16 v[36:39], v[160:163], v[168:171], v[36:39]
	v_mfma_f32_16x16x32_bf16 v[64:67], v[156:159], v[196:199], v[64:67]
	v_mfma_f32_16x16x32_bf16 v[60:63], v[164:167], v[196:199], v[60:63]
	v_mfma_f32_16x16x32_bf16 v[56:59], v[156:159], v[192:195], v[56:59]
	v_mfma_f32_16x16x32_bf16 v[52:55], v[164:167], v[192:195], v[52:55]
	v_mfma_f32_16x16x32_bf16 v[48:51], v[156:159], v[188:191], v[48:51]
	v_mfma_f32_16x16x32_bf16 v[44:47], v[164:167], v[188:191], v[44:47]
	v_mfma_f32_16x16x32_bf16 v[40:43], v[156:159], v[184:187], v[40:43]
	v_mfma_f32_16x16x32_bf16 v[36:39], v[164:167], v[184:187], v[36:39]
	s_setprio 0
	s_setprio 1
	v_mfma_f32_16x16x32_bf16 v[32:35], v[136:139], v[180:183], v[32:35]
	v_mfma_f32_16x16x32_bf16 v[28:31], v[144:147], v[180:183], v[28:31]
	v_mfma_f32_16x16x32_bf16 v[24:27], v[136:139], v[176:179], v[24:27]
	v_mfma_f32_16x16x32_bf16 v[20:23], v[144:147], v[176:179], v[20:23]
	v_mfma_f32_16x16x32_bf16 v[16:19], v[136:139], v[172:175], v[16:19]
	v_mfma_f32_16x16x32_bf16 v[12:15], v[144:147], v[172:175], v[12:15]
	v_mfma_f32_16x16x32_bf16 v[8:11], v[136:139], v[168:171], v[8:11]
	v_mfma_f32_16x16x32_bf16 v[4:7], v[144:147], v[168:171], v[4:7]
	v_mfma_f32_16x16x32_bf16 v[32:35], v[140:143], v[196:199], v[32:35]
	v_mfma_f32_16x16x32_bf16 v[28:31], v[148:151], v[196:199], v[28:31]
	v_mfma_f32_16x16x32_bf16 v[24:27], v[140:143], v[192:195], v[24:27]
	v_mfma_f32_16x16x32_bf16 v[20:23], v[148:151], v[192:195], v[20:23]
	v_mfma_f32_16x16x32_bf16 v[16:19], v[140:143], v[188:191], v[16:19]
	v_mfma_f32_16x16x32_bf16 v[12:15], v[148:151], v[188:191], v[12:15]
	v_mfma_f32_16x16x32_bf16 v[8:11], v[140:143], v[184:187], v[8:11]
	v_mfma_f32_16x16x32_bf16 v[4:7], v[148:151], v[184:187], v[4:7]
	s_setprio 0
.LBB0_1315:
	s_barrier
	v_add_u32_e32 v136, 0x18000, v241
	v_add_u32_e32 v148, 0x1c000, v241
	ds_read_b128 v[152:155], v136
	ds_read_b128 v[156:159], v136 offset:1024
	ds_read_b128 v[160:163], v136 offset:2048
	ds_read_b128 v[164:167], v136 offset:3072
	ds_read_b128 v[136:139], v148
	ds_read_b128 v[140:143], v148 offset:1024
	ds_read_b128 v[144:147], v148 offset:2048
	ds_read_b128 v[148:151], v148 offset:3072
	s_mov_b32 m0, s70
	s_waitcnt lgkmcnt(0)
	ds_read_b128 v[180:183], v242 offset:32768
	ds_read_b128 v[196:199], v242 offset:33792
	ds_read_b128 v[176:179], v242 offset:34816
	ds_read_b128 v[192:195], v242 offset:35840
	ds_read_b128 v[172:175], v242 offset:36864
	ds_read_b128 v[188:191], v242 offset:37888
	ds_read_b128 v[168:171], v242 offset:38912
	ds_read_b128 v[184:187], v242 offset:39936
	global_load_lds_dwordx4 v218, s[56:57]
	s_mov_b32 m0, s71
	s_nop 0
	global_load_lds_dwordx4 v219, s[56:57]
	s_waitcnt vmcnt(8)
	s_waitcnt lgkmcnt(0)
	s_barrier
	s_setprio 1
	v_mfma_f32_16x16x32_bf16 v[132:135], v[152:155], v[180:183], v[132:135]
	v_mfma_f32_16x16x32_bf16 v[128:131], v[160:163], v[180:183], v[128:131]
	v_mfma_f32_16x16x32_bf16 v[124:127], v[152:155], v[176:179], v[124:127]
	v_mfma_f32_16x16x32_bf16 v[120:123], v[160:163], v[176:179], v[120:123]
	v_mfma_f32_16x16x32_bf16 v[116:119], v[152:155], v[172:175], v[116:119]
	v_mfma_f32_16x16x32_bf16 v[112:115], v[160:163], v[172:175], v[112:115]
	v_mfma_f32_16x16x32_bf16 v[108:111], v[152:155], v[168:171], v[108:111]
	v_mfma_f32_16x16x32_bf16 v[104:107], v[160:163], v[168:171], v[104:107]
	v_mfma_f32_16x16x32_bf16 v[132:135], v[156:159], v[196:199], v[132:135]
	v_mfma_f32_16x16x32_bf16 v[128:131], v[164:167], v[196:199], v[128:131]
	v_mfma_f32_16x16x32_bf16 v[124:127], v[156:159], v[192:195], v[124:127]
	v_mfma_f32_16x16x32_bf16 v[120:123], v[164:167], v[192:195], v[120:123]
	v_mfma_f32_16x16x32_bf16 v[116:119], v[156:159], v[188:191], v[116:119]
	v_mfma_f32_16x16x32_bf16 v[112:115], v[164:167], v[188:191], v[112:115]
	v_mfma_f32_16x16x32_bf16 v[108:111], v[156:159], v[184:187], v[108:111]
	v_mfma_f32_16x16x32_bf16 v[104:107], v[164:167], v[184:187], v[104:107]
	s_setprio 0
	s_setprio 1
	v_mfma_f32_16x16x32_bf16 v[100:103], v[136:139], v[180:183], v[100:103]
	v_mfma_f32_16x16x32_bf16 v[96:99], v[144:147], v[180:183], v[96:99]
	v_mfma_f32_16x16x32_bf16 v[92:95], v[136:139], v[176:179], v[92:95]
	v_mfma_f32_16x16x32_bf16 v[88:91], v[144:147], v[176:179], v[88:91]
	v_mfma_f32_16x16x32_bf16 v[80:83], v[136:139], v[172:175], v[80:83]
	v_mfma_f32_16x16x32_bf16 v[76:79], v[144:147], v[172:175], v[76:79]
	v_mfma_f32_16x16x32_bf16 v[72:75], v[136:139], v[168:171], v[72:75]
	v_mfma_f32_16x16x32_bf16 v[68:71], v[144:147], v[168:171], v[68:71]
	v_mfma_f32_16x16x32_bf16 v[100:103], v[140:143], v[196:199], v[100:103]
	v_mfma_f32_16x16x32_bf16 v[96:99], v[148:151], v[196:199], v[96:99]
	v_mfma_f32_16x16x32_bf16 v[92:95], v[140:143], v[192:195], v[92:95]
	v_mfma_f32_16x16x32_bf16 v[88:91], v[148:151], v[192:195], v[88:91]
	v_mfma_f32_16x16x32_bf16 v[80:83], v[140:143], v[188:191], v[80:83]
	v_mfma_f32_16x16x32_bf16 v[76:79], v[148:151], v[188:191], v[76:79]
	v_mfma_f32_16x16x32_bf16 v[72:75], v[140:143], v[184:187], v[72:75]
	v_mfma_f32_16x16x32_bf16 v[68:71], v[148:151], v[184:187], v[68:71]
	s_setprio 0
	s_barrier
	s_and_b64 vcc, exec, s[4:5]
	s_cbranch_vccnz .LBB0_1317
	ds_read_b128 v[180:183], v242 offset:49152
	ds_read_b128 v[196:199], v242 offset:50176
	ds_read_b128 v[176:179], v242 offset:51200
	ds_read_b128 v[192:195], v242 offset:52224
	ds_read_b128 v[172:175], v242 offset:53248
	ds_read_b128 v[188:191], v242 offset:54272
	ds_read_b128 v[168:171], v242 offset:55296
	ds_read_b128 v[184:187], v242 offset:56320
.LBB0_1317:
	v_mov_b32_e32 v213, v3
	v_lshl_add_u64 v[204:205], s[56:57], 0, v[2:3]
	v_lshl_add_u64 v[206:207], s[56:57], 0, v[212:213]
	s_add_u32 s56, s54, 0x8000
	s_addc_u32 s57, s55, 0
	s_mov_b32 m0, s72
	v_lshl_add_u64 v[200:201], s[56:57], 0, v[208:209]
	s_add_u32 s54, s54, 0xc000
	global_load_lds_dwordx4 v[200:201], off
	v_lshl_add_u64 v[200:201], s[56:57], 0, v[210:211]
	s_mov_b32 m0, s73
	s_addc_u32 s55, s55, 0
	global_load_lds_dwordx4 v[200:201], off
	v_lshl_add_u64 v[200:201], s[54:55], 0, v[208:209]
	s_mov_b32 m0, s76
	s_and_b64 vcc, exec, s[4:5]
	global_load_lds_dwordx4 v[200:201], off
	v_lshl_add_u64 v[200:201], s[54:55], 0, v[210:211]
	s_mov_b32 m0, s77
	s_nop 0
	global_load_lds_dwordx4 v[200:201], off
	v_lshl_add_u64 v[200:201], v[204:205], 0, s[36:37]
	s_mov_b32 m0, s74
	s_nop 0
	global_load_lds_dwordx4 v[200:201], off
	v_lshl_add_u64 v[200:201], v[206:207], 0, s[36:37]
	s_mov_b32 m0, s75
	s_nop 0
	global_load_lds_dwordx4 v[200:201], off
	s_waitcnt vmcnt(8)
	s_waitcnt lgkmcnt(0)
	s_barrier
	s_cbranch_vccnz .LBB0_1308
	s_setprio 1
	v_mfma_f32_16x16x32_bf16 v[64:67], v[152:155], v[180:183], v[64:67]
	v_mfma_f32_16x16x32_bf16 v[60:63], v[160:163], v[180:183], v[60:63]
	v_mfma_f32_16x16x32_bf16 v[56:59], v[152:155], v[176:179], v[56:59]
	v_mfma_f32_16x16x32_bf16 v[52:55], v[160:163], v[176:179], v[52:55]
	v_mfma_f32_16x16x32_bf16 v[48:51], v[152:155], v[172:175], v[48:51]
	v_mfma_f32_16x16x32_bf16 v[44:47], v[160:163], v[172:175], v[44:47]
	v_mfma_f32_16x16x32_bf16 v[40:43], v[152:155], v[168:171], v[40:43]
	v_mfma_f32_16x16x32_bf16 v[36:39], v[160:163], v[168:171], v[36:39]
	v_mfma_f32_16x16x32_bf16 v[64:67], v[156:159], v[196:199], v[64:67]
	v_mfma_f32_16x16x32_bf16 v[60:63], v[164:167], v[196:199], v[60:63]
	v_mfma_f32_16x16x32_bf16 v[56:59], v[156:159], v[192:195], v[56:59]
	v_mfma_f32_16x16x32_bf16 v[52:55], v[164:167], v[192:195], v[52:55]
	v_mfma_f32_16x16x32_bf16 v[48:51], v[156:159], v[188:191], v[48:51]
	v_mfma_f32_16x16x32_bf16 v[44:47], v[164:167], v[188:191], v[44:47]
	v_mfma_f32_16x16x32_bf16 v[40:43], v[156:159], v[184:187], v[40:43]
	v_mfma_f32_16x16x32_bf16 v[36:39], v[164:167], v[184:187], v[36:39]
	s_setprio 0
	s_setprio 1
	v_mfma_f32_16x16x32_bf16 v[32:35], v[136:139], v[180:183], v[32:35]
	v_mfma_f32_16x16x32_bf16 v[28:31], v[144:147], v[180:183], v[28:31]
	v_mfma_f32_16x16x32_bf16 v[24:27], v[136:139], v[176:179], v[24:27]
	v_mfma_f32_16x16x32_bf16 v[20:23], v[144:147], v[176:179], v[20:23]
	v_mfma_f32_16x16x32_bf16 v[16:19], v[136:139], v[172:175], v[16:19]
	v_mfma_f32_16x16x32_bf16 v[12:15], v[144:147], v[172:175], v[12:15]
	v_mfma_f32_16x16x32_bf16 v[8:11], v[136:139], v[168:171], v[8:11]
	v_mfma_f32_16x16x32_bf16 v[4:7], v[144:147], v[168:171], v[4:7]
	v_mfma_f32_16x16x32_bf16 v[32:35], v[140:143], v[196:199], v[32:35]
	v_mfma_f32_16x16x32_bf16 v[28:31], v[148:151], v[196:199], v[28:31]
	v_mfma_f32_16x16x32_bf16 v[24:27], v[140:143], v[192:195], v[24:27]
	v_mfma_f32_16x16x32_bf16 v[20:23], v[148:151], v[192:195], v[20:23]
	v_mfma_f32_16x16x32_bf16 v[16:19], v[140:143], v[188:191], v[16:19]
	v_mfma_f32_16x16x32_bf16 v[12:15], v[148:151], v[188:191], v[12:15]
	v_mfma_f32_16x16x32_bf16 v[8:11], v[140:143], v[184:187], v[8:11]
	v_mfma_f32_16x16x32_bf16 v[4:7], v[148:151], v[184:187], v[4:7]
	s_setprio 0
	s_branch .LBB0_1308

.LBB0_1429:
	s_add_u32 s52, s48, 0x80
	s_addc_u32 s53, s49, 0
	s_and_b64 s[50:51], s[50:51], exec
	s_cselect_b32 s51, s15, s74
	s_cselect_b32 s50, s39, s73
	s_mov_b32 m0, s55
	s_cselect_b32 s53, s25, s53
	s_cselect_b32 s52, s24, s52
	v_lshl_add_u64 v[200:201], s[50:51], 0, v[208:209]
	s_add_u32 s76, s50, 0x4000
	global_load_lds_dwordx4 v[200:201], off
	v_lshl_add_u64 v[200:201], s[50:51], 0, v[210:211]
	s_mov_b32 m0, s56
	s_addc_u32 s77, s51, 0
	global_load_lds_dwordx4 v[200:201], off
	v_lshl_add_u64 v[200:201], s[76:77], 0, v[208:209]
	s_mov_b32 m0, s57
	s_and_b64 vcc, exec, s[4:5]
	global_load_lds_dwordx4 v[200:201], off
	v_lshl_add_u64 v[200:201], s[76:77], 0, v[210:211]
	s_mov_b32 m0, s59
	s_nop 0
	global_load_lds_dwordx4 v[200:201], off
	s_mov_b32 m0, s7
	s_nop 0
	global_load_lds_dwordx4 v2, s[52:53]
	s_mov_b32 m0, s60
	s_nop 0
	global_load_lds_dwordx4 v212, s[52:53]
	s_waitcnt vmcnt(8)
	s_waitcnt lgkmcnt(0)
	s_barrier
	s_cbranch_vccnz .LBB0_1431
	s_setprio 1
	v_mfma_f32_16x16x32_bf16 v[64:67], v[152:155], v[180:183], v[64:67]
	v_mfma_f32_16x16x32_bf16 v[60:63], v[160:163], v[180:183], v[60:63]
	v_mfma_f32_16x16x32_bf16 v[56:59], v[152:155], v[176:179], v[56:59]
	v_mfma_f32_16x16x32_bf16 v[52:55], v[160:163], v[176:179], v[52:55]
	v_mfma_f32_16x16x32_bf16 v[48:51], v[152:155], v[172:175], v[48:51]
	v_mfma_f32_16x16x32_bf16 v[44:47], v[160:163], v[172:175], v[44:47]
	v_mfma_f32_16x16x32_bf16 v[40:43], v[152:155], v[168:171], v[40:43]
	v_mfma_f32_16x16x32_bf16 v[36:39], v[160:163], v[168:171], v[36:39]
	v_mfma_f32_16x16x32_bf16 v[64:67], v[156:159], v[196:199], v[64:67]
	v_mfma_f32_16x16x32_bf16 v[60:63], v[164:167], v[196:199], v[60:63]
	v_mfma_f32_16x16x32_bf16 v[56:59], v[156:159], v[192:195], v[56:59]
	v_mfma_f32_16x16x32_bf16 v[52:55], v[164:167], v[192:195], v[52:55]
	v_mfma_f32_16x16x32_bf16 v[48:51], v[156:159], v[188:191], v[48:51]
	v_mfma_f32_16x16x32_bf16 v[44:47], v[164:167], v[188:191], v[44:47]
	v_mfma_f32_16x16x32_bf16 v[40:43], v[156:159], v[184:187], v[40:43]
	v_mfma_f32_16x16x32_bf16 v[36:39], v[164:167], v[184:187], v[36:39]
	s_setprio 0
	s_setprio 1
	v_mfma_f32_16x16x32_bf16 v[32:35], v[136:139], v[180:183], v[32:35]
	v_mfma_f32_16x16x32_bf16 v[28:31], v[144:147], v[180:183], v[28:31]
	v_mfma_f32_16x16x32_bf16 v[24:27], v[136:139], v[176:179], v[24:27]
	v_mfma_f32_16x16x32_bf16 v[20:23], v[144:147], v[176:179], v[20:23]
	v_mfma_f32_16x16x32_bf16 v[16:19], v[136:139], v[172:175], v[16:19]
	v_mfma_f32_16x16x32_bf16 v[12:15], v[144:147], v[172:175], v[12:15]
	v_mfma_f32_16x16x32_bf16 v[8:11], v[136:139], v[168:171], v[8:11]
	v_mfma_f32_16x16x32_bf16 v[4:7], v[144:147], v[168:171], v[4:7]
	v_mfma_f32_16x16x32_bf16 v[32:35], v[140:143], v[196:199], v[32:35]
	v_mfma_f32_16x16x32_bf16 v[28:31], v[148:151], v[196:199], v[28:31]
	v_mfma_f32_16x16x32_bf16 v[24:27], v[140:143], v[192:195], v[24:27]
	v_mfma_f32_16x16x32_bf16 v[20:23], v[148:151], v[192:195], v[20:23]
	v_mfma_f32_16x16x32_bf16 v[16:19], v[140:143], v[188:191], v[16:19]
	v_mfma_f32_16x16x32_bf16 v[12:15], v[148:151], v[188:191], v[12:15]
	v_mfma_f32_16x16x32_bf16 v[8:11], v[140:143], v[184:187], v[8:11]
	v_mfma_f32_16x16x32_bf16 v[4:7], v[148:151], v[184:187], v[4:7]
	s_setprio 0
.LBB0_1431:
	s_barrier
	v_add_u32_e32 v136, 0x18000, v241
	v_add_u32_e32 v148, 0x1c000, v241
	ds_read_b128 v[152:155], v136
	ds_read_b128 v[156:159], v136 offset:1024
	ds_read_b128 v[160:163], v136 offset:2048
	ds_read_b128 v[164:167], v136 offset:3072
	ds_read_b128 v[136:139], v148
	ds_read_b128 v[140:143], v148 offset:1024
	ds_read_b128 v[144:147], v148 offset:2048
	ds_read_b128 v[148:151], v148 offset:3072
	s_mov_b32 m0, s61
	s_waitcnt lgkmcnt(0)
	ds_read_b128 v[180:183], v242 offset:32768
	ds_read_b128 v[196:199], v242 offset:33792
	ds_read_b128 v[176:179], v242 offset:34816
	ds_read_b128 v[192:195], v242 offset:35840
	ds_read_b128 v[172:175], v242 offset:36864
	ds_read_b128 v[188:191], v242 offset:37888
	ds_read_b128 v[168:171], v242 offset:38912
	ds_read_b128 v[184:187], v242 offset:39936
	global_load_lds_dwordx4 v218, s[52:53]
	s_mov_b32 m0, s62
	s_nop 0
	global_load_lds_dwordx4 v219, s[52:53]
	s_waitcnt vmcnt(8)
	s_waitcnt lgkmcnt(0)
	s_barrier
	s_setprio 1
	v_mfma_f32_16x16x32_bf16 v[132:135], v[152:155], v[180:183], v[132:135]
	v_mfma_f32_16x16x32_bf16 v[128:131], v[160:163], v[180:183], v[128:131]
	v_mfma_f32_16x16x32_bf16 v[124:127], v[152:155], v[176:179], v[124:127]
	v_mfma_f32_16x16x32_bf16 v[120:123], v[160:163], v[176:179], v[120:123]
	v_mfma_f32_16x16x32_bf16 v[116:119], v[152:155], v[172:175], v[116:119]
	v_mfma_f32_16x16x32_bf16 v[112:115], v[160:163], v[172:175], v[112:115]
	v_mfma_f32_16x16x32_bf16 v[108:111], v[152:155], v[168:171], v[108:111]
	v_mfma_f32_16x16x32_bf16 v[104:107], v[160:163], v[168:171], v[104:107]
	v_mfma_f32_16x16x32_bf16 v[132:135], v[156:159], v[196:199], v[132:135]
	v_mfma_f32_16x16x32_bf16 v[128:131], v[164:167], v[196:199], v[128:131]
	v_mfma_f32_16x16x32_bf16 v[124:127], v[156:159], v[192:195], v[124:127]
	v_mfma_f32_16x16x32_bf16 v[120:123], v[164:167], v[192:195], v[120:123]
	v_mfma_f32_16x16x32_bf16 v[116:119], v[156:159], v[188:191], v[116:119]
	v_mfma_f32_16x16x32_bf16 v[112:115], v[164:167], v[188:191], v[112:115]
	v_mfma_f32_16x16x32_bf16 v[108:111], v[156:159], v[184:187], v[108:111]
	v_mfma_f32_16x16x32_bf16 v[104:107], v[164:167], v[184:187], v[104:107]
	s_setprio 0
	s_setprio 1
	v_mfma_f32_16x16x32_bf16 v[100:103], v[136:139], v[180:183], v[100:103]
	v_mfma_f32_16x16x32_bf16 v[96:99], v[144:147], v[180:183], v[96:99]
	v_mfma_f32_16x16x32_bf16 v[92:95], v[136:139], v[176:179], v[92:95]
	v_mfma_f32_16x16x32_bf16 v[88:91], v[144:147], v[176:179], v[88:91]
	v_mfma_f32_16x16x32_bf16 v[80:83], v[136:139], v[172:175], v[80:83]
	v_mfma_f32_16x16x32_bf16 v[76:79], v[144:147], v[172:175], v[76:79]
	v_mfma_f32_16x16x32_bf16 v[72:75], v[136:139], v[168:171], v[72:75]
	v_mfma_f32_16x16x32_bf16 v[68:71], v[144:147], v[168:171], v[68:71]
	v_mfma_f32_16x16x32_bf16 v[100:103], v[140:143], v[196:199], v[100:103]
	v_mfma_f32_16x16x32_bf16 v[96:99], v[148:151], v[196:199], v[96:99]
	v_mfma_f32_16x16x32_bf16 v[92:95], v[140:143], v[192:195], v[92:95]
	v_mfma_f32_16x16x32_bf16 v[88:91], v[148:151], v[192:195], v[88:91]
	v_mfma_f32_16x16x32_bf16 v[80:83], v[140:143], v[188:191], v[80:83]
	v_mfma_f32_16x16x32_bf16 v[76:79], v[148:151], v[188:191], v[76:79]
	v_mfma_f32_16x16x32_bf16 v[72:75], v[140:143], v[184:187], v[72:75]
	v_mfma_f32_16x16x32_bf16 v[68:71], v[148:151], v[184:187], v[68:71]
	s_setprio 0
	s_barrier
	s_and_b64 vcc, exec, s[4:5]
	s_cbranch_vccnz .LBB0_1433
	ds_read_b128 v[180:183], v242 offset:49152
	ds_read_b128 v[196:199], v242 offset:50176
	ds_read_b128 v[176:179], v242 offset:51200
	ds_read_b128 v[192:195], v242 offset:52224
	ds_read_b128 v[172:175], v242 offset:53248
	ds_read_b128 v[188:191], v242 offset:54272
	ds_read_b128 v[168:171], v242 offset:55296
	ds_read_b128 v[184:187], v242 offset:56320
.LBB0_1433:
	v_mov_b32_e32 v213, v3
	v_lshl_add_u64 v[200:201], s[52:53], 0, v[2:3]
	v_lshl_add_u64 v[204:205], s[52:53], 0, v[212:213]
	s_add_u32 s52, s50, 0x8000
	s_addc_u32 s53, s51, 0
	s_mov_b32 m0, s63
	v_lshl_add_u64 v[206:207], s[52:53], 0, v[208:209]
	s_add_u32 s50, s50, 0xc000
	global_load_lds_dwordx4 v[206:207], off
	v_lshl_add_u64 v[206:207], s[52:53], 0, v[210:211]
	s_mov_b32 m0, s64
	s_addc_u32 s51, s51, 0
	global_load_lds_dwordx4 v[206:207], off
	v_lshl_add_u64 v[206:207], s[50:51], 0, v[208:209]
	s_mov_b32 m0, s67
	v_lshl_add_u64 v[200:201], v[200:201], 0, s[36:37]
	global_load_lds_dwordx4 v[206:207], off
	v_lshl_add_u64 v[206:207], s[50:51], 0, v[210:211]
	s_mov_b32 m0, s68
	s_and_b64 vcc, exec, s[4:5]
	global_load_lds_dwordx4 v[206:207], off
	s_mov_b32 m0, s65
	s_nop 0
	global_load_lds_dwordx4 v[200:201], off
	v_lshl_add_u64 v[200:201], v[204:205], 0, s[36:37]
	s_mov_b32 m0, s66
	s_nop 0
	global_load_lds_dwordx4 v[200:201], off
	s_waitcnt vmcnt(8)
	s_waitcnt lgkmcnt(0)
	s_barrier
	s_cbranch_vccnz .LBB0_1424
	s_setprio 1
	v_mfma_f32_16x16x32_bf16 v[64:67], v[152:155], v[180:183], v[64:67]
	v_mfma_f32_16x16x32_bf16 v[60:63], v[160:163], v[180:183], v[60:63]
	v_mfma_f32_16x16x32_bf16 v[56:59], v[152:155], v[176:179], v[56:59]
	v_mfma_f32_16x16x32_bf16 v[52:55], v[160:163], v[176:179], v[52:55]
	v_mfma_f32_16x16x32_bf16 v[48:51], v[152:155], v[172:175], v[48:51]
	v_mfma_f32_16x16x32_bf16 v[44:47], v[160:163], v[172:175], v[44:47]
	v_mfma_f32_16x16x32_bf16 v[40:43], v[152:155], v[168:171], v[40:43]
	v_mfma_f32_16x16x32_bf16 v[36:39], v[160:163], v[168:171], v[36:39]
	v_mfma_f32_16x16x32_bf16 v[64:67], v[156:159], v[196:199], v[64:67]
	v_mfma_f32_16x16x32_bf16 v[60:63], v[164:167], v[196:199], v[60:63]
	v_mfma_f32_16x16x32_bf16 v[56:59], v[156:159], v[192:195], v[56:59]
	v_mfma_f32_16x16x32_bf16 v[52:55], v[164:167], v[192:195], v[52:55]
	v_mfma_f32_16x16x32_bf16 v[48:51], v[156:159], v[188:191], v[48:51]
	v_mfma_f32_16x16x32_bf16 v[44:47], v[164:167], v[188:191], v[44:47]
	v_mfma_f32_16x16x32_bf16 v[40:43], v[156:159], v[184:187], v[40:43]
	v_mfma_f32_16x16x32_bf16 v[36:39], v[164:167], v[184:187], v[36:39]
	s_setprio 0
	s_setprio 1
	v_mfma_f32_16x16x32_bf16 v[32:35], v[136:139], v[180:183], v[32:35]
	v_mfma_f32_16x16x32_bf16 v[28:31], v[144:147], v[180:183], v[28:31]
	v_mfma_f32_16x16x32_bf16 v[24:27], v[136:139], v[176:179], v[24:27]
	v_mfma_f32_16x16x32_bf16 v[20:23], v[144:147], v[176:179], v[20:23]
	v_mfma_f32_16x16x32_bf16 v[16:19], v[136:139], v[172:175], v[16:19]
	v_mfma_f32_16x16x32_bf16 v[12:15], v[144:147], v[172:175], v[12:15]
	v_mfma_f32_16x16x32_bf16 v[8:11], v[136:139], v[168:171], v[8:11]
	v_mfma_f32_16x16x32_bf16 v[4:7], v[144:147], v[168:171], v[4:7]
	v_mfma_f32_16x16x32_bf16 v[32:35], v[140:143], v[196:199], v[32:35]
	v_mfma_f32_16x16x32_bf16 v[28:31], v[148:151], v[196:199], v[28:31]
	v_mfma_f32_16x16x32_bf16 v[24:27], v[140:143], v[192:195], v[24:27]
	v_mfma_f32_16x16x32_bf16 v[20:23], v[148:151], v[192:195], v[20:23]
	v_mfma_f32_16x16x32_bf16 v[16:19], v[140:143], v[188:191], v[16:19]
	v_mfma_f32_16x16x32_bf16 v[12:15], v[148:151], v[188:191], v[12:15]
	v_mfma_f32_16x16x32_bf16 v[8:11], v[140:143], v[184:187], v[8:11]
	v_mfma_f32_16x16x32_bf16 v[4:7], v[148:151], v[184:187], v[4:7]
	s_setprio 0
	s_branch .LBB0_1424
